# gather: IDX/GW prefetch issued at the u/v boundary of the previous token; no vmcnt wait in the pre section
# baseline (speedup 1.0000x reference)
; __device__ __forceinline__ int fresh_lane() { unsigned z = 0u; asm volatile("" : "+v"(z)); return (int)__builtin_amdgcn_mbcnt_hi(~0u, __builtin_amdgcn_mbcnt_lo(~0u, z)); }
; #define GATHER_ISSUE(k, sn_) do { const int sn = (sn_); const int secn = (sn >> 6) & 3; \
;         const int idsel = (sn >= 256) ? id0n : ((secn & 1) ? id1 : id0); \
;         const unsigned so = (unsigned)__builtin_amdgcn_readlane(idsel, sn & 63) * ROW4 + ((secn >= 2) ? TAB4 : 0u); \
;         ring[k] = __builtin_bit_cast(v4u, __builtin_amdgcn_raw_buffer_load_b128(rs, voff, so, 0)); } while (0)
;     const unsigned char* UV4 = (const unsigned char*)(F.ws + WS_UB) + (size_t)layer * (2u * TAB4);
;     const bf16* ZB = (const bf16*)(F.ws + WS_ZF); const bf16* PLE = (const bf16*)(F.ws + WS_PLE);
;     const int* IDX = (const int*)(F.ws + WS_IDX); const float* GWt = (const float*)(F.ws + WS_GW);
;     float* OF = (layer == 3 && !dummy) ? F.out : (float*)nullptr; bf16* XB = (bf16*)(F.ws + (dummy ? WS_X1B : WS_XB));
;     ...
;     const int idmask = (dummy == 1) ? PROBE_GATHER_MASK : 0x3fff;
;     ...
;     const float* gain1 = F.ln_gain + (size_t)(layer * 2) * D; const float* bias1 = F.ln_bias + (size_t)(layer * 2) * D;
;     const float* gain = F.ln_gain + (size_t)(layer * 2 + 1) * D; const float* bias = F.ln_bias + (size_t)(layer * 2 + 1) * D;
;     const int lane = fresh_lane();
;     const bool b3 = (lane & 8) != 0, b2 = (lane & 4) != 0, b1 = (lane & 2) != 0, b0 = (lane & 1) != 0;
;     const __amdgpu_buffer_rsrc_t rs = __builtin_amdgcn_make_buffer_rsrc((void*)UV4, (short)0, (int)(2u * TAB4), 0x00020000);
;     const unsigned voff = (unsigned)lane * 16u;
;     v4u ring[16];
;     int id0 = 0, id1 = 0, id0n = 0;
;     ...
;     int id1n = 0; float g0n = 0.f, g1n = 0.f;
;     if (F.gw < T) { gather_sorted_ids(IDX, GWt, F.gw, lane, id0n, id1n, g0n, g1n);
;     ...
;         id0n &= idmask; id1n &= idmask;
;     ...
; #pragma unroll
;         for (int k = 0; k < 16; ++k) GATHER_ISSUE(k, 256 + k); }
.LBB0_1412:
	s_andn2_b64 vcc, exec, s[14:15]
	s_cbranch_vccnz .LBB0_1452
	s_add_u32 s8, s60, 0x4a600000
	v_writelane_b32 v254, s8, 56
	s_addc_u32 s8, s61, 0
	v_writelane_b32 v255, s8, 5
	s_add_u32 s8, s60, 0x66600000
	v_writelane_b32 v255, s8, 7
	s_addc_u32 s8, s61, 0
	s_cmp_eq_u32 s18, 3
	v_writelane_b32 v255, s8, 9
	s_cselect_b64 s[8:9], -1, 0
	s_add_u32 s10, s60, 0x36600000
	v_writelane_b32 v255, s10, 11
	s_addc_u32 s43, s61, 0
	s_lshl_b32 s10, s18, 1
	s_mov_b64 s[16:17], s[80:81]
	v_writelane_b32 v255, s76, 1
	s_mov_b64 s[18:19], s[82:83]
	s_mov_b64 s[20:21], s[84:85]
	s_mov_b64 s[22:23], s[86:87]
	v_writelane_b32 v255, s77, 2
	v_readlane_b32 s76, v254, 1
	s_ashr_i32 s11, s10, 31
	v_readlane_b32 s90, v254, 15
	v_readlane_b32 s91, v254, 16
	s_lshl_b64 s[12:13], s[10:11], 13
	s_mov_b64 s[14:15], s[90:91]
	s_add_u32 s36, s14, s12
	s_addc_u32 s37, s15, s13
	s_add_u32 s12, s16, s12
	s_addc_u32 s13, s17, s13
	s_or_b32 s10, s10, 1
	v_readlane_b32 s72, v255, 1
	s_ashr_i32 s11, s10, 31
	v_readlane_b32 s73, v255, 2
	v_writelane_b32 v255, s12, 13
	s_lshl_b64 s[10:11], s[10:11], 13
	v_readlane_b32 s80, v254, 5
	v_writelane_b32 v255, s13, 14
	s_add_u32 s12, s14, s10
	s_addc_u32 s13, s15, s11
	v_readlane_b32 s81, v254, 6
	s_add_u32 s80, s16, s10
	s_addc_u32 s81, s17, s11
	v_readlane_b32 s10, v254, 51
	v_readlane_b32 s82, v254, 7
	v_readlane_b32 s83, v254, 8
	v_readlane_b32 s11, v254, 52
	s_and_b64 s[82:83], s[8:9], s[10:11]
	s_add_u32 s30, s60, 0x57600000
	v_writelane_b32 v255, s12, 15
	s_addc_u32 s39, s61, 0
	s_add_u32 s8, s60, 0x53200000
	v_writelane_b32 v255, s13, 16
	v_writelane_b32 v255, s8, 33
	s_addc_u32 s8, s61, 0
	v_writelane_b32 v255, s8, 35
	s_add_u32 s8, s60, 0x53600000
	v_writelane_b32 v255, s8, 29
	s_addc_u32 s8, s61, 0
	v_cmp_eq_u32_e64 s[28:29], 0, v68
	v_cmp_eq_u32_e32 vcc, 0, v67
	v_writelane_b32 v255, s8, 31
	s_xor_b64 s[44:45], vcc, s[28:29]
	v_cmp_eq_u32_e64 s[20:21], 0, v69
	v_writelane_b32 v255, s44, 17
	v_lshlrev_b32_e32 v70, 5, v130
	v_ashrrev_i32_e32 v71, 31, v70
	v_writelane_b32 v255, s45, 18
	s_xor_b64 s[44:45], vcc, s[20:21]
	v_writelane_b32 v255, s44, 19
	v_add_u32_e32 v194, 4, v66
	v_add_u32_e32 v195, 8, v66
	v_writelane_b32 v255, s45, 20
	s_xor_b64 s[44:45], vcc, s[0:1]
	v_writelane_b32 v255, s44, 21
	v_add_u32_e32 v196, 12, v66
	v_lshl_add_u64 v[66:67], s[60:61], 0, v[70:71]
	v_writelane_b32 v255, s45, 22
	s_xor_b64 s[44:45], vcc, s[2:3]
	v_writelane_b32 v255, s44, 23
	s_xor_b64 s[8:9], s[4:5], s[6:7]
	s_xor_b64 s[10:11], s[2:3], s[4:5]
	v_writelane_b32 v255, s45, 24
	s_xor_b64 s[44:45], vcc, s[4:5]
	v_writelane_b32 v255, s44, 25
	s_xor_b64 s[12:13], s[2:3], s[6:7]
	s_xor_b64 s[14:15], s[0:1], s[2:3]
	v_writelane_b32 v255, s45, 26
	s_xor_b64 s[44:45], vcc, s[6:7]
	v_writelane_b32 v255, s44, 27
	s_xor_b64 s[16:17], s[0:1], s[4:5]
	s_xor_b64 s[18:19], s[0:1], s[6:7]
	v_writelane_b32 v255, s45, 28
	s_mov_b64 s[44:45], 0x55600000
	s_xor_b64 s[22:23], s[20:21], s[0:1]
	s_xor_b64 s[24:25], s[20:21], s[2:3]
	s_xor_b64 s[26:27], s[20:21], s[4:5]
	v_ashrrev_i32_e32 v193, 4, v130
	v_lshl_add_u64 v[132:133], v[66:67], 0, s[44:45]
	s_xor_b64 s[44:45], s[20:21], s[6:7]
	s_xor_b64 s[46:47], s[28:29], s[20:21]
	s_xor_b64 s[48:49], s[28:29], s[0:1]
	s_xor_b64 s[50:51], s[28:29], s[2:3]
	s_xor_b64 s[52:53], s[28:29], s[4:5]
	s_xor_b64 s[54:55], s[28:29], s[6:7]
	v_readlane_b32 s77, v254, 2
	v_readlane_b32 s78, v254, 3
	v_readlane_b32 s79, v254, 4
	v_readlane_b32 s84, v254, 9
	v_readlane_b32 s85, v254, 10
	v_readlane_b32 s86, v254, 11
	v_readlane_b32 s87, v254, 12
	v_readlane_b32 s88, v254, 13
	v_readlane_b32 s89, v254, 14
	v_readlane_b32 s98, v254, 55
	s_lshl_b32 s98, s98, 6
	v_add_u32_e32 v228, s98, v130
	v_lshlrev_b32_e32 v228, 4, v228
	global_load_dwordx4 v[212:215], v228, s[36:37]
	global_load_dwordx4 v[224:227], v228, s[80:81]
	v_readlane_b32 s98, v255, 13
	v_readlane_b32 s99, v255, 14
	s_nop 4
	global_load_dwordx4 v[216:219], v228, s[98:99]
	v_readlane_b32 s98, v255, 15
	v_readlane_b32 s99, v255, 16
	s_nop 4
	global_load_dwordx4 v[220:223], v228, s[98:99]
	s_waitcnt vmcnt(3)
	ds_write_b128 v228, v[212:215]
	s_waitcnt vmcnt(2)
	ds_write_b128 v228, v[224:227] offset:24576
	s_waitcnt vmcnt(1)
	ds_write_b128 v228, v[216:219] offset:8192
	s_waitcnt vmcnt(0)
	ds_write_b128 v228, v[220:223] offset:16384
	s_waitcnt lgkmcnt(0)
	s_barrier
	v_readlane_b32 s100, v254, 58
	v_readlane_b32 s99, v255, 1
	s_add_i32 s99, s100, s99
	s_cmp_lt_i32 s99, 0x4000
	s_cselect_b32 s99, s99, s100
	s_lshl_b32 s100, s100, 12
	s_lshl_b32 s99, s99, 9
	v_lshl_add_u32 v244, v130, 6, s100
	v_lshl_add_u32 v249, v130, 2, s99
	v_readlane_b32 s100, v255, 7
	v_readlane_b32 s101, v255, 9
	s_nop 4
	global_load_dwordx4 v[212:215], v244, s[100:101] offset:48
	global_load_dwordx4 v[216:219], v244, s[100:101] offset:32
	global_load_dwordx4 v[220:223], v244, s[100:101] offset:16
	global_load_dwordx4 v[224:227], v244, s[100:101]
	v_readlane_b32 s100, v254, 56
	v_readlane_b32 s101, v255, 5
	s_nop 4
	global_load_dwordx4 v[228:231], v244, s[100:101] offset:48
	global_load_dwordx4 v[232:235], v244, s[100:101] offset:32
	global_load_dwordx4 v[236:239], v244, s[100:101] offset:16
	global_load_dwordx4 v[240:243], v244, s[100:101]
	global_load_dword v245, v249, s[70:71] offset:256
	global_load_dword v246, v249, s[40:41] offset:256
	global_load_dword v247, v249, s[40:41]
	global_load_dword v248, v249, s[70:71]
	s_waitcnt vmcnt(0)
	s_branch .LBB0_1416

; __device__ __forceinline__ int shx_i(int v, int m, int lane) { return __builtin_amdgcn_ds_bpermute((lane ^ m) << 2, v); }
; __device__ __forceinline__ void gather_sorted_ids(const int* IDX, const float* GWt, int t, int lane, int& id0, int& id1, float& g0, float& g1) {
;     const int ia = IDX[(size_t)t * 128 + lane], ib = IDX[(size_t)t * 128 + 64 + lane];
;     const float ga = GWt[(size_t)t * 128 + lane], gb = GWt[(size_t)t * 128 + 64 + lane];
;     unsigned a = ((unsigned)ia << 16) | (unsigned)fminf(ga * 65536.0f, 65535.0f), b = ((unsigned)ib << 16) | (unsigned)fminf(gb * 65536.0f, 65535.0f);
; #pragma unroll
;     for (int k = 2; k <= 128; k <<= 1) {
;         if (k == 128) { const unsigned mn = a < b ? a : b, mx = a < b ? b : a; a = mn; b = mx; }
; #pragma unroll
;         for (int j = (k >= 128 ? 32 : k >> 1); j > 0; j >>= 1) {
;             const bool lower = (lane & j) == 0;
;             const bool upa = (k >= 128) ? true : ((lane & k) == 0);
;             const bool upb = (k >= 128) ? true : (k == 64 ? false : ((lane & k) == 0));
;             const unsigned oa = (unsigned)shx_i((int)a, j, lane), ob = (unsigned)shx_i((int)b, j, lane);
;             a = (lower == upa) ? (a < oa ? a : oa) : (a < oa ? oa : a);
;             b = (lower == upb) ? (b < ob ? b : ob) : (b < ob ? ob : b);
;         }
;     }
;     ...
;         { const int tn = (t + F.ngw < T) ? t + F.ngw : t; gather_sorted_ids(IDX, GWt, tn, lane, id0n, id1n, g0n, g1n);
.LBB0_1418:
	s_add_i32 s62, s88, s72
	s_cmpk_gt_i32 s62, 0x3fff
	s_mov_b32 s56, s62
	s_cselect_b64 s[84:85], -1, 0
	s_cmpk_lt_i32 s62, 0x4000
	v_writelane_b32 v254, s56, 58
	s_nop 1
	v_writelane_b32 v254, s57, 59
	s_cselect_b32 s56, s62, s88
	s_ashr_i32 s57, s56, 31
	s_lshl_b64 s[56:57], s[56:57], 7
	v_lshl_add_u64 v[84:85], s[56:57], 0, v[130:131]
	v_lshlrev_b64 v[84:85], 2, v[84:85]
	s_mov_b64 s[56:57], 0x100
	v_lshl_add_u64 v[86:87], v[84:85], 0, s[56:57]
	v_lshl_add_u64 v[88:89], s[70:71], 0, v[86:87]
	v_lshl_add_u64 v[86:87], s[40:41], 0, v[86:87]
	v_mov_b32_e32 v69, v245
	v_mov_b32_e32 v81, v246
	v_lshl_add_u64 v[86:87], s[70:71], 0, v[84:85]
	v_lshl_add_u64 v[84:85], s[40:41], 0, v[84:85]
	v_readlane_b32 s56, v255, 17
	v_readlane_b32 s57, v255, 18
	v_mov_b32_e32 v83, v247
	v_mul_f32_e32 v81, 0x47800000, v81
	v_min_f32_e32 v81, 0x477fff00, v81
	v_cvt_u32_f32_e32 v81, v81
	v_mul_f32_e32 v83, 0x47800000, v83
	v_lshl_or_b32 v69, v69, 16, v81
	v_mov_b32_e32 v81, v248
	ds_bpermute_b32 v84, v163, v69
	v_min_f32_e32 v83, 0x477fff00, v83
	v_cvt_u32_f32_e32 v83, v83
	v_lshl_or_b32 v81, v81, 16, v83
	ds_bpermute_b32 v83, v163, v81
	s_waitcnt lgkmcnt(0)
	v_min_u32_e32 v85, v81, v83
	v_max_u32_e32 v81, v81, v83
	v_min_u32_e32 v83, v69, v84
	v_max_u32_e32 v69, v69, v84
	v_cndmask_b32_e64 v81, v85, v81, s[8:9]
	v_cndmask_b32_e64 v69, v83, v69, s[8:9]
	ds_bpermute_b32 v83, v188, v81
	ds_bpermute_b32 v84, v188, v69
	s_waitcnt lgkmcnt(1)
	v_min_u32_e32 v85, v81, v83
	v_max_u32_e32 v81, v81, v83
	s_waitcnt lgkmcnt(0)
	v_min_u32_e32 v83, v69, v84
	v_max_u32_e32 v69, v69, v84
	v_cndmask_b32_e64 v81, v85, v81, s[10:11]
	v_cndmask_b32_e64 v69, v83, v69, s[10:11]
	ds_bpermute_b32 v83, v163, v81
	ds_bpermute_b32 v84, v163, v69
	s_waitcnt lgkmcnt(1)
	v_min_u32_e32 v85, v81, v83
	v_max_u32_e32 v81, v81, v83
	s_waitcnt lgkmcnt(0)
	v_min_u32_e32 v83, v69, v84
	v_max_u32_e32 v69, v69, v84
	v_cndmask_b32_e64 v81, v85, v81, s[12:13]
	v_cndmask_b32_e64 v69, v83, v69, s[12:13]
	ds_bpermute_b32 v83, v189, v81
	ds_bpermute_b32 v84, v189, v69
	s_waitcnt lgkmcnt(1)
	v_min_u32_e32 v85, v81, v83
	v_max_u32_e32 v81, v81, v83
	s_waitcnt lgkmcnt(0)
	v_min_u32_e32 v83, v69, v84
	v_max_u32_e32 v69, v69, v84
	v_cndmask_b32_e64 v81, v85, v81, s[14:15]
	v_cndmask_b32_e64 v69, v83, v69, s[14:15]
	ds_bpermute_b32 v83, v188, v81
	ds_bpermute_b32 v84, v188, v69
	s_waitcnt lgkmcnt(1)
	v_min_u32_e32 v85, v81, v83
	v_max_u32_e32 v81, v81, v83
	s_waitcnt lgkmcnt(0)
	v_min_u32_e32 v83, v69, v84
	v_max_u32_e32 v69, v69, v84
	v_cndmask_b32_e64 v81, v85, v81, s[16:17]
	v_cndmask_b32_e64 v69, v83, v69, s[16:17]
	ds_bpermute_b32 v83, v163, v81
	ds_bpermute_b32 v84, v163, v69
	s_waitcnt lgkmcnt(1)
	v_min_u32_e32 v85, v81, v83
	v_max_u32_e32 v81, v81, v83
	s_waitcnt lgkmcnt(0)
	v_min_u32_e32 v83, v69, v84
	v_max_u32_e32 v69, v69, v84
	v_cndmask_b32_e64 v81, v85, v81, s[18:19]
	v_cndmask_b32_e64 v69, v83, v69, s[18:19]
	ds_bpermute_b32 v83, v190, v81
	ds_bpermute_b32 v84, v190, v69
	s_waitcnt lgkmcnt(1)
	v_min_u32_e32 v85, v81, v83
	v_max_u32_e32 v81, v81, v83
	s_waitcnt lgkmcnt(0)
	v_min_u32_e32 v83, v69, v84
	v_max_u32_e32 v69, v69, v84
	v_cndmask_b32_e64 v81, v85, v81, s[22:23]
	v_cndmask_b32_e64 v69, v83, v69, s[22:23]
	ds_bpermute_b32 v83, v189, v81
	ds_bpermute_b32 v84, v189, v69
	s_waitcnt lgkmcnt(1)
	v_min_u32_e32 v85, v81, v83
	v_max_u32_e32 v81, v81, v83
	s_waitcnt lgkmcnt(0)
	v_min_u32_e32 v83, v69, v84
	v_max_u32_e32 v69, v69, v84
	v_cndmask_b32_e64 v81, v85, v81, s[24:25]
	v_cndmask_b32_e64 v69, v83, v69, s[24:25]
	ds_bpermute_b32 v83, v188, v81
	ds_bpermute_b32 v84, v188, v69
	s_waitcnt lgkmcnt(1)
	v_min_u32_e32 v85, v81, v83
	v_max_u32_e32 v81, v81, v83
	s_waitcnt lgkmcnt(0)
	v_min_u32_e32 v83, v69, v84
	v_max_u32_e32 v69, v69, v84
	v_cndmask_b32_e64 v81, v85, v81, s[26:27]
	v_cndmask_b32_e64 v69, v83, v69, s[26:27]
	ds_bpermute_b32 v83, v163, v81
	ds_bpermute_b32 v84, v163, v69
	s_waitcnt lgkmcnt(1)
	v_min_u32_e32 v85, v81, v83
	v_max_u32_e32 v81, v81, v83
	s_waitcnt lgkmcnt(0)
	v_min_u32_e32 v83, v69, v84
	v_max_u32_e32 v69, v69, v84
	v_cndmask_b32_e64 v81, v85, v81, s[44:45]
	v_cndmask_b32_e64 v69, v83, v69, s[44:45]
	ds_bpermute_b32 v83, v191, v81
	ds_bpermute_b32 v84, v191, v69
	s_waitcnt lgkmcnt(1)
	v_min_u32_e32 v85, v81, v83
	v_max_u32_e32 v81, v81, v83
	s_waitcnt lgkmcnt(0)
	v_min_u32_e32 v83, v69, v84
	v_max_u32_e32 v69, v69, v84
	v_cndmask_b32_e64 v81, v85, v81, s[46:47]
	v_cndmask_b32_e64 v69, v83, v69, s[46:47]
	ds_bpermute_b32 v83, v190, v81
	ds_bpermute_b32 v84, v190, v69
	s_waitcnt lgkmcnt(1)
	v_min_u32_e32 v85, v81, v83
	v_max_u32_e32 v81, v81, v83
	s_waitcnt lgkmcnt(0)
	v_min_u32_e32 v83, v69, v84
	v_max_u32_e32 v69, v69, v84
	v_cndmask_b32_e64 v81, v85, v81, s[48:49]
	v_cndmask_b32_e64 v69, v83, v69, s[48:49]
	ds_bpermute_b32 v83, v189, v81
	ds_bpermute_b32 v84, v189, v69
	s_waitcnt lgkmcnt(1)
; __device__ __forceinline__ int shx_i(int v, int m, int lane) { return __builtin_amdgcn_ds_bpermute((lane ^ m) << 2, v); }
; __device__ __forceinline__ void gather_sorted_ids(const int* IDX, const float* GWt, int t, int lane, int& id0, int& id1, float& g0, float& g1) {
;     ...
; #pragma unroll
;     for (int k = 2; k <= 128; k <<= 1) {
;         if (k == 128) { const unsigned mn = a < b ? a : b, mx = a < b ? b : a; a = mn; b = mx; }
; #pragma unroll
;         for (int j = (k >= 128 ? 32 : k >> 1); j > 0; j >>= 1) {
;             const bool lower = (lane & j) == 0;
;             const bool upa = (k >= 128) ? true : ((lane & k) == 0);
;             const bool upb = (k >= 128) ? true : (k == 64 ? false : ((lane & k) == 0));
;             const unsigned oa = (unsigned)shx_i((int)a, j, lane), ob = (unsigned)shx_i((int)b, j, lane);
;             a = (lower == upa) ? (a < oa ? a : oa) : (a < oa ? oa : a);
;             b = (lower == upb) ? (b < ob ? b : ob) : (b < ob ? ob : b);
;         }
;     }
;     id0 = (int)(a >> 16); id1 = (int)(b >> 16);
;     g0 = ((float)(a & 0xffffu) + 0.5f) * (1.0f / 65536.0f); g1 = ((float)(b & 0xffffu) + 0.5f) * (1.0f / 65536.0f);
	v_min_u32_e32 v85, v81, v83
	v_max_u32_e32 v81, v81, v83
	s_waitcnt lgkmcnt(0)
	v_min_u32_e32 v83, v69, v84
	v_max_u32_e32 v69, v69, v84
	v_cndmask_b32_e64 v81, v85, v81, s[50:51]
	v_cndmask_b32_e64 v69, v83, v69, s[50:51]
	ds_bpermute_b32 v83, v188, v81
	ds_bpermute_b32 v84, v188, v69
	s_waitcnt lgkmcnt(1)
	v_min_u32_e32 v85, v81, v83
	v_max_u32_e32 v81, v81, v83
	s_waitcnt lgkmcnt(0)
	v_min_u32_e32 v83, v69, v84
	v_max_u32_e32 v69, v69, v84
	v_cndmask_b32_e64 v81, v85, v81, s[52:53]
	v_cndmask_b32_e64 v69, v83, v69, s[52:53]
	ds_bpermute_b32 v83, v163, v81
	ds_bpermute_b32 v84, v163, v69
	s_waitcnt lgkmcnt(1)
	v_min_u32_e32 v85, v81, v83
	v_max_u32_e32 v81, v81, v83
	s_waitcnt lgkmcnt(0)
	v_min_u32_e32 v83, v69, v84
	v_max_u32_e32 v69, v69, v84
	v_cndmask_b32_e64 v81, v85, v81, s[54:55]
	v_cndmask_b32_e64 v69, v83, v69, s[54:55]
	ds_bpermute_b32 v83, v192, v81
	ds_bpermute_b32 v84, v192, v69
	s_waitcnt lgkmcnt(1)
	v_min_u32_e32 v85, v81, v83
	v_max_u32_e32 v81, v81, v83
	s_waitcnt lgkmcnt(0)
	v_min_u32_e32 v83, v69, v84
	v_max_u32_e32 v69, v69, v84
	v_cndmask_b32_e64 v81, v85, v81, s[56:57]
	v_cndmask_b32_e64 v69, v83, v69, s[28:29]
	ds_bpermute_b32 v83, v191, v81
	ds_bpermute_b32 v84, v191, v69
	v_readlane_b32 s56, v255, 19
	v_readlane_b32 s57, v255, 20
	s_waitcnt lgkmcnt(1)
	v_min_u32_e32 v85, v81, v83
	v_max_u32_e32 v81, v81, v83
	s_waitcnt lgkmcnt(0)
	v_min_u32_e32 v83, v69, v84
	v_max_u32_e32 v69, v69, v84
	v_cndmask_b32_e64 v81, v85, v81, s[56:57]
	v_cndmask_b32_e64 v69, v83, v69, s[20:21]
	ds_bpermute_b32 v83, v190, v81
	ds_bpermute_b32 v84, v190, v69
	v_readlane_b32 s56, v255, 21
	v_readlane_b32 s57, v255, 22
	s_waitcnt lgkmcnt(1)
	v_min_u32_e32 v85, v81, v83
	v_max_u32_e32 v81, v81, v83
	s_waitcnt lgkmcnt(0)
	v_min_u32_e32 v83, v69, v84
	v_max_u32_e32 v69, v69, v84
	v_cndmask_b32_e64 v81, v85, v81, s[56:57]
	v_cndmask_b32_e64 v69, v83, v69, s[0:1]
	ds_bpermute_b32 v83, v189, v81
	ds_bpermute_b32 v84, v189, v69
	v_readlane_b32 s56, v255, 23
	v_readlane_b32 s57, v255, 24
	s_waitcnt lgkmcnt(1)
	v_min_u32_e32 v85, v81, v83
	v_max_u32_e32 v81, v81, v83
	s_waitcnt lgkmcnt(0)
	v_min_u32_e32 v83, v69, v84
	v_max_u32_e32 v69, v69, v84
	v_cndmask_b32_e64 v81, v85, v81, s[56:57]
	v_cndmask_b32_e64 v69, v83, v69, s[2:3]
	ds_bpermute_b32 v83, v188, v81
	ds_bpermute_b32 v84, v188, v69
	v_readlane_b32 s56, v255, 25
	v_readlane_b32 s57, v255, 26
	s_waitcnt lgkmcnt(1)
	v_min_u32_e32 v85, v81, v83
	v_max_u32_e32 v81, v81, v83
	s_waitcnt lgkmcnt(0)
	v_min_u32_e32 v83, v69, v84
	v_max_u32_e32 v69, v69, v84
	v_cndmask_b32_e64 v81, v85, v81, s[56:57]
	v_cndmask_b32_e64 v69, v83, v69, s[4:5]
	ds_bpermute_b32 v83, v163, v81
	ds_bpermute_b32 v84, v163, v69
	v_readlane_b32 s56, v255, 27
	v_readlane_b32 s57, v255, 28
	s_waitcnt lgkmcnt(1)
	v_max_u32_e32 v85, v81, v83
	v_min_u32_e32 v81, v81, v83
	s_waitcnt lgkmcnt(0)
	v_max_u32_e32 v83, v69, v84
	v_min_u32_e32 v69, v69, v84
	v_cndmask_b32_e64 v81, v81, v85, s[56:57]
	v_cndmask_b32_e64 v69, v69, v83, s[6:7]
	v_max_u32_e32 v83, v81, v69
	v_min_u32_e32 v69, v81, v69
	ds_bpermute_b32 v81, v192, v69
	ds_bpermute_b32 v84, v192, v83
	s_mov_b32 s56, 0
	s_mov_b32 s57, 31
	s_waitcnt lgkmcnt(1)
	v_min_u32_e32 v85, v69, v81
	v_max_u32_e32 v69, v69, v81
	v_cndmask_b32_e64 v69, v69, v85, s[28:29]
	s_waitcnt lgkmcnt(0)
	v_min_u32_e32 v81, v83, v84
	v_max_u32_e32 v83, v83, v84
	v_cndmask_b32_e64 v81, v83, v81, s[28:29]
	ds_bpermute_b32 v83, v191, v69
	ds_bpermute_b32 v84, v191, v81
	s_waitcnt lgkmcnt(1)
	v_min_u32_e32 v85, v69, v83
	v_max_u32_e32 v69, v69, v83
	v_cndmask_b32_e64 v69, v69, v85, s[20:21]
	s_waitcnt lgkmcnt(0)
	v_min_u32_e32 v83, v81, v84
	v_max_u32_e32 v81, v81, v84
	v_cndmask_b32_e64 v81, v81, v83, s[20:21]
	ds_bpermute_b32 v83, v190, v69
	ds_bpermute_b32 v84, v190, v81
	s_waitcnt lgkmcnt(1)
	v_min_u32_e32 v85, v69, v83
	v_max_u32_e32 v69, v69, v83
	v_cndmask_b32_e64 v69, v69, v85, s[0:1]
	s_waitcnt lgkmcnt(0)
	v_min_u32_e32 v83, v81, v84
	v_max_u32_e32 v81, v81, v84
	v_cndmask_b32_e64 v81, v81, v83, s[0:1]
	ds_bpermute_b32 v83, v189, v69
	ds_bpermute_b32 v84, v189, v81
	s_waitcnt lgkmcnt(1)
	v_min_u32_e32 v85, v69, v83
	v_max_u32_e32 v69, v69, v83
	v_cndmask_b32_e64 v69, v69, v85, s[2:3]
	s_waitcnt lgkmcnt(0)
	v_min_u32_e32 v83, v81, v84
	v_max_u32_e32 v81, v81, v84
	v_cndmask_b32_e64 v81, v81, v83, s[2:3]
	ds_bpermute_b32 v83, v188, v69
	ds_bpermute_b32 v84, v188, v81
	s_waitcnt lgkmcnt(1)
	v_min_u32_e32 v85, v69, v83
	v_max_u32_e32 v69, v69, v83
	v_cndmask_b32_e64 v105, v69, v85, s[4:5]
	s_waitcnt lgkmcnt(0)
	v_min_u32_e32 v69, v81, v84
	v_max_u32_e32 v81, v81, v84
	v_cndmask_b32_e64 v197, v81, v69, s[4:5]
	ds_bpermute_b32 v106, v163, v105
	ds_bpermute_b32 v198, v163, v197
	v_mov_b32_e32 v81, 0
	s_waitcnt vmcnt(0)

.Lnb_1421:
.LBB0_1421:
	v_mov_b32_e32 v69, v1
	v_mov_b32_e32 v83, v1
	s_waitcnt vmcnt(6)
	v_dot8c_i32_i4_e32 v69, v6, v74
	v_dot8c_i32_i4_e32 v83, v6, v70
	v_dot8c_i32_i4_e32 v69, v7, v75
	v_dot8c_i32_i4_e32 v83, v7, v71
	v_dot8c_i32_i4_e32 v69, v8, v76
	v_dot8c_i32_i4_e32 v83, v8, v72
	s_add_i32 s62, s57, -15
	v_dot8c_i32_i4_e32 v69, v9, v77
	v_dot8c_i32_i4_e32 v83, v9, v73
	s_bitcmp0_b32 s62, 6
	s_cselect_b64 vcc, -1, 0
	s_nop 0
	v_lshl_add_u32 v6, v69, 4, v83
	v_cvt_f32_i32_e32 v69, v6
	v_cndmask_b32_e32 v6, v79, v78, vcc
	s_nop 0
	v_readlane_b32 s62, v6, s62
	s_lshl_b32 s63, s62, 10
	s_cmp_gt_u32 s56, 2
	s_cselect_b32 s62, 0x1000000, 0
	s_add_i32 s63, s63, s62
	buffer_load_dwordx4 v[6:9], v0, s[92:95], s63 offen
	v_mov_b32_e32 v83, v1
	v_mov_b32_e32 v84, v1
	s_waitcnt vmcnt(6)
	v_dot8c_i32_i4_e32 v83, v14, v74
	v_dot8c_i32_i4_e32 v84, v14, v70
	v_dot8c_i32_i4_e32 v83, v15, v75
	v_dot8c_i32_i4_e32 v84, v15, v71
	v_dot8c_i32_i4_e32 v83, v16, v76
	v_dot8c_i32_i4_e32 v84, v16, v72
	s_add_i32 s63, s57, -14
	v_dot8c_i32_i4_e32 v83, v17, v77
	v_dot8c_i32_i4_e32 v84, v17, v73
	s_bitcmp0_b32 s63, 6
	s_cselect_b64 vcc, -1, 0
	s_nop 0
	v_lshl_add_u32 v14, v83, 4, v84
	v_cvt_f32_i32_e32 v83, v14
	v_cndmask_b32_e32 v14, v79, v78, vcc
	s_nop 0
	v_readlane_b32 s63, v14, s63
	s_lshl_b32 s63, s63, 10
	s_add_i32 s63, s63, s62
	s_nop 2
	buffer_load_dwordx4 v[14:17], v0, s[92:95], s63 offen
	v_mov_b32_e32 v84, v1
	v_mov_b32_e32 v85, v1
	s_waitcnt vmcnt(6)
	v_dot8c_i32_i4_e32 v84, v30, v74
	v_dot8c_i32_i4_e32 v85, v30, v70
	v_dot8c_i32_i4_e32 v84, v31, v75
	v_dot8c_i32_i4_e32 v85, v31, v71
	v_dot8c_i32_i4_e32 v84, v32, v76
	v_dot8c_i32_i4_e32 v85, v32, v72
	s_add_i32 s63, s57, -13
	v_dot8c_i32_i4_e32 v84, v33, v77
	v_dot8c_i32_i4_e32 v85, v33, v73
	s_bitcmp0_b32 s63, 6
	s_cselect_b64 vcc, -1, 0
	s_nop 0
	v_lshl_add_u32 v30, v84, 4, v85
	v_cvt_f32_i32_e32 v84, v30
	v_cndmask_b32_e32 v30, v79, v78, vcc
	s_nop 0
	v_readlane_b32 s63, v30, s63
	s_lshl_b32 s63, s63, 10
	s_add_i32 s63, s63, s62
	s_nop 2
	buffer_load_dwordx4 v[30:33], v0, s[92:95], s63 offen
	v_mov_b32_e32 v85, v1
	v_mov_b32_e32 v86, v1
	s_waitcnt vmcnt(6)
	v_dot8c_i32_i4_e32 v85, v46, v74
	v_dot8c_i32_i4_e32 v86, v46, v70
	v_dot8c_i32_i4_e32 v85, v47, v75
	v_dot8c_i32_i4_e32 v86, v47, v71
	v_dot8c_i32_i4_e32 v85, v48, v76
	v_dot8c_i32_i4_e32 v86, v48, v72
	s_add_i32 s63, s57, -12
	v_dot8c_i32_i4_e32 v85, v49, v77
	v_dot8c_i32_i4_e32 v86, v49, v73
	s_bitcmp0_b32 s63, 6
	s_cselect_b64 vcc, -1, 0
	s_nop 0
	v_lshl_add_u32 v46, v85, 4, v86
	v_cvt_f32_i32_e32 v85, v46
	v_cndmask_b32_e32 v46, v79, v78, vcc
	s_nop 0
	v_readlane_b32 s63, v46, s63
	s_lshl_b32 s63, s63, 10
	s_add_i32 s63, s63, s62
	s_nop 2
	buffer_load_dwordx4 v[46:49], v0, s[92:95], s63 offen
	v_mov_b32_e32 v86, v1
	v_mov_b32_e32 v87, v1
	s_waitcnt vmcnt(6)
	v_dot8c_i32_i4_e32 v86, v2, v74
	v_dot8c_i32_i4_e32 v87, v2, v70
	v_dot8c_i32_i4_e32 v86, v3, v75
	v_dot8c_i32_i4_e32 v87, v3, v71
	v_dot8c_i32_i4_e32 v86, v4, v76
	v_dot8c_i32_i4_e32 v87, v4, v72
	s_add_i32 s63, s57, -11
	v_dot8c_i32_i4_e32 v86, v5, v77
	v_dot8c_i32_i4_e32 v87, v5, v73
	s_bitcmp0_b32 s63, 6
	s_cselect_b64 vcc, -1, 0
	s_nop 0
	v_lshl_add_u32 v2, v86, 4, v87
	v_cvt_f32_i32_e32 v86, v2
	v_cndmask_b32_e32 v2, v79, v78, vcc
	s_nop 0
	v_readlane_b32 s63, v2, s63
	s_lshl_b32 s63, s63, 10
	s_add_i32 s63, s63, s62
	s_nop 2
	buffer_load_dwordx4 v[2:5], v0, s[92:95], s63 offen
	v_mov_b32_e32 v87, v1
	v_mov_b32_e32 v88, v1
	s_waitcnt vmcnt(6)
	v_dot8c_i32_i4_e32 v87, v22, v74
	v_dot8c_i32_i4_e32 v88, v22, v70
	v_dot8c_i32_i4_e32 v87, v23, v75
	v_dot8c_i32_i4_e32 v88, v23, v71
	v_dot8c_i32_i4_e32 v87, v24, v76
	v_dot8c_i32_i4_e32 v88, v24, v72
	s_add_i32 s63, s57, -10
	v_dot8c_i32_i4_e32 v87, v25, v77
	v_dot8c_i32_i4_e32 v88, v25, v73
	s_bitcmp0_b32 s63, 6
	s_cselect_b64 vcc, -1, 0
	s_nop 0
	v_lshl_add_u32 v22, v87, 4, v88
	v_cvt_f32_i32_e32 v87, v22
	v_cndmask_b32_e32 v22, v79, v78, vcc
	s_nop 0
	v_readlane_b32 s63, v22, s63
	s_lshl_b32 s63, s63, 10
	s_add_i32 s63, s63, s62
	s_nop 2
	buffer_load_dwordx4 v[22:25], v0, s[92:95], s63 offen
	v_mov_b32_e32 v88, v1
	v_mov_b32_e32 v89, v1
	s_waitcnt vmcnt(6)
	v_dot8c_i32_i4_e32 v88, v38, v74
	v_dot8c_i32_i4_e32 v89, v38, v70
	v_dot8c_i32_i4_e32 v88, v39, v75
	v_dot8c_i32_i4_e32 v89, v39, v71
	v_dot8c_i32_i4_e32 v88, v40, v76
	v_dot8c_i32_i4_e32 v89, v40, v72
	s_add_i32 s63, s57, -9
	v_dot8c_i32_i4_e32 v88, v41, v77
	v_dot8c_i32_i4_e32 v89, v41, v73
	s_bitcmp0_b32 s63, 6
	s_cselect_b64 vcc, -1, 0
	s_nop 0
	v_lshl_add_u32 v38, v88, 4, v89
	v_cvt_f32_i32_e32 v88, v38
	v_cndmask_b32_e32 v38, v79, v78, vcc
	s_nop 0
	v_readlane_b32 s63, v38, s63
	s_lshl_b32 s63, s63, 10
	s_add_i32 s63, s63, s62
	s_nop 2
	buffer_load_dwordx4 v[38:41], v0, s[92:95], s63 offen
	v_mov_b32_e32 v89, v1
	v_mov_b32_e32 v90, v1
	s_waitcnt vmcnt(6)
	v_dot8c_i32_i4_e32 v89, v54, v74
	v_dot8c_i32_i4_e32 v90, v54, v70
	v_dot8c_i32_i4_e32 v89, v55, v75
	v_dot8c_i32_i4_e32 v90, v55, v71
	v_dot8c_i32_i4_e32 v89, v56, v76
	v_dot8c_i32_i4_e32 v90, v56, v72
	s_add_i32 s63, s57, -8
	v_dot8c_i32_i4_e32 v89, v57, v77
	v_dot8c_i32_i4_e32 v90, v57, v73
	s_bitcmp0_b32 s63, 6
	s_cselect_b64 vcc, -1, 0
	s_nop 0
	v_lshl_add_u32 v54, v89, 4, v90
	v_cvt_f32_i32_e32 v89, v54
	v_cndmask_b32_e32 v54, v79, v78, vcc
	s_nop 0
	v_readlane_b32 s63, v54, s63
	s_lshl_b32 s63, s63, 10
	s_add_i32 s63, s63, s62
	s_nop 2
	buffer_load_dwordx4 v[54:57], v0, s[92:95], s63 offen
	v_mov_b32_e32 v90, v1
	v_mov_b32_e32 v91, v1
	s_waitcnt vmcnt(6)
	v_dot8c_i32_i4_e32 v90, v10, v74
	v_dot8c_i32_i4_e32 v91, v10, v70
	v_dot8c_i32_i4_e32 v90, v11, v75
	v_dot8c_i32_i4_e32 v91, v11, v71
	v_dot8c_i32_i4_e32 v90, v12, v76
	v_dot8c_i32_i4_e32 v91, v12, v72
	s_add_i32 s63, s57, -7
	v_dot8c_i32_i4_e32 v90, v13, v77
	v_dot8c_i32_i4_e32 v91, v13, v73
	s_bitcmp0_b32 s63, 6
	s_cselect_b64 vcc, -1, 0
	s_nop 0
	v_lshl_add_u32 v10, v90, 4, v91
	v_cvt_f32_i32_e32 v90, v10
	v_cndmask_b32_e32 v10, v79, v78, vcc
	s_nop 0
	v_readlane_b32 s63, v10, s63
	s_lshl_b32 s63, s63, 10
	s_add_i32 s63, s63, s62
	s_nop 2
	buffer_load_dwordx4 v[10:13], v0, s[92:95], s63 offen
	v_mov_b32_e32 v91, v1
	v_mov_b32_e32 v92, v1
	s_waitcnt vmcnt(6)
	v_dot8c_i32_i4_e32 v91, v26, v74
	v_dot8c_i32_i4_e32 v92, v26, v70
	v_dot8c_i32_i4_e32 v91, v27, v75
	v_dot8c_i32_i4_e32 v92, v27, v71
	v_dot8c_i32_i4_e32 v91, v28, v76
	v_dot8c_i32_i4_e32 v92, v28, v72
	s_add_i32 s63, s57, -6
	v_dot8c_i32_i4_e32 v91, v29, v77
	v_dot8c_i32_i4_e32 v92, v29, v73
	s_bitcmp0_b32 s63, 6
	s_cselect_b64 vcc, -1, 0
	s_nop 0
	v_lshl_add_u32 v26, v91, 4, v92
	v_cvt_f32_i32_e32 v91, v26
	v_cndmask_b32_e32 v26, v79, v78, vcc
	s_nop 0
	v_readlane_b32 s63, v26, s63
	s_lshl_b32 s63, s63, 10
	s_add_i32 s63, s63, s62
	s_nop 2
	buffer_load_dwordx4 v[26:29], v0, s[92:95], s63 offen
	v_mov_b32_e32 v92, v1
	v_mov_b32_e32 v93, v1
	s_waitcnt vmcnt(6)
	v_dot8c_i32_i4_e32 v92, v42, v74
	v_dot8c_i32_i4_e32 v93, v42, v70
	v_dot8c_i32_i4_e32 v92, v43, v75
	v_dot8c_i32_i4_e32 v93, v43, v71
	v_dot8c_i32_i4_e32 v92, v44, v76
	v_dot8c_i32_i4_e32 v93, v44, v72
	s_add_i32 s63, s57, -5
	v_dot8c_i32_i4_e32 v92, v45, v77
	v_dot8c_i32_i4_e32 v93, v45, v73
	s_bitcmp0_b32 s63, 6
	s_cselect_b64 vcc, -1, 0
	s_nop 0
	v_lshl_add_u32 v42, v92, 4, v93
	v_cvt_f32_i32_e32 v92, v42
	v_cndmask_b32_e32 v42, v79, v78, vcc
	s_nop 0
	v_readlane_b32 s63, v42, s63
	s_lshl_b32 s63, s63, 10
	s_add_i32 s63, s63, s62
	s_nop 2
	buffer_load_dwordx4 v[42:45], v0, s[92:95], s63 offen
	v_mov_b32_e32 v93, v1
	v_mov_b32_e32 v94, v1
	s_waitcnt vmcnt(6)
	v_dot8c_i32_i4_e32 v93, v58, v74
	v_dot8c_i32_i4_e32 v94, v58, v70
	v_dot8c_i32_i4_e32 v93, v59, v75
	v_dot8c_i32_i4_e32 v94, v59, v71
	v_dot8c_i32_i4_e32 v93, v60, v76
	v_dot8c_i32_i4_e32 v94, v60, v72
	s_add_i32 s63, s57, -4
	v_dot8c_i32_i4_e32 v93, v61, v77
	v_dot8c_i32_i4_e32 v94, v61, v73
	s_bitcmp0_b32 s63, 6
	s_cselect_b64 vcc, -1, 0
	s_nop 0
	v_lshl_add_u32 v58, v93, 4, v94
	v_cvt_f32_i32_e32 v93, v58
	v_cndmask_b32_e32 v58, v79, v78, vcc
	s_nop 0
	v_readlane_b32 s63, v58, s63
	s_lshl_b32 s63, s63, 10
	s_add_i32 s63, s63, s62
	s_nop 2
	buffer_load_dwordx4 v[58:61], v0, s[92:95], s63 offen
	v_mov_b32_e32 v94, v1
	v_mov_b32_e32 v95, v1
	s_waitcnt vmcnt(6)
	v_dot8c_i32_i4_e32 v94, v18, v74
	v_dot8c_i32_i4_e32 v95, v18, v70
	v_dot8c_i32_i4_e32 v94, v19, v75
	v_dot8c_i32_i4_e32 v95, v19, v71
	v_dot8c_i32_i4_e32 v94, v20, v76
	v_dot8c_i32_i4_e32 v95, v20, v72
	s_add_i32 s63, s57, -3
	v_dot8c_i32_i4_e32 v94, v21, v77
	v_dot8c_i32_i4_e32 v95, v21, v73
	s_bitcmp0_b32 s63, 6
	s_cselect_b64 vcc, -1, 0
	s_nop 0
	v_lshl_add_u32 v18, v94, 4, v95
	v_cvt_f32_i32_e32 v94, v18
	v_cndmask_b32_e32 v18, v79, v78, vcc
	s_nop 0
	v_readlane_b32 s63, v18, s63
	s_lshl_b32 s63, s63, 10
	s_add_i32 s63, s63, s62
	s_nop 2
	buffer_load_dwordx4 v[18:21], v0, s[92:95], s63 offen
	v_mov_b32_e32 v95, v1
	v_mov_b32_e32 v96, v1
	s_waitcnt vmcnt(6)
	v_dot8c_i32_i4_e32 v95, v34, v74
	v_dot8c_i32_i4_e32 v96, v34, v70
	v_dot8c_i32_i4_e32 v95, v35, v75
	v_dot8c_i32_i4_e32 v96, v35, v71
	v_dot8c_i32_i4_e32 v95, v36, v76
	v_dot8c_i32_i4_e32 v96, v36, v72
	s_add_i32 s63, s57, -2
	v_dot8c_i32_i4_e32 v95, v37, v77
	v_dot8c_i32_i4_e32 v96, v37, v73
	s_bitcmp0_b32 s63, 6
	s_cselect_b64 vcc, -1, 0
	s_nop 0
	v_lshl_add_u32 v34, v95, 4, v96
	v_cvt_f32_i32_e32 v95, v34
	v_cndmask_b32_e32 v34, v79, v78, vcc
	s_nop 0
	v_readlane_b32 s63, v34, s63
	s_lshl_b32 s63, s63, 10
	s_add_i32 s63, s63, s62
	s_nop 2
	buffer_load_dwordx4 v[34:37], v0, s[92:95], s63 offen
	v_mov_b32_e32 v96, v1
	v_mov_b32_e32 v97, v1
	s_waitcnt vmcnt(6)
	v_dot8c_i32_i4_e32 v96, v50, v74
	v_dot8c_i32_i4_e32 v97, v50, v70
	v_dot8c_i32_i4_e32 v96, v51, v75
	v_dot8c_i32_i4_e32 v97, v51, v71
	v_dot8c_i32_i4_e32 v96, v52, v76
	v_dot8c_i32_i4_e32 v97, v52, v72
	s_add_i32 s63, s57, -1
	v_dot8c_i32_i4_e32 v96, v53, v77
	v_dot8c_i32_i4_e32 v97, v53, v73
	s_bitcmp0_b32 s63, 6
	s_cselect_b64 vcc, -1, 0
	s_nop 0
	v_lshl_add_u32 v50, v96, 4, v97
	v_cvt_f32_i32_e32 v96, v50
	v_cndmask_b32_e32 v50, v79, v78, vcc
	s_nop 0
	v_readlane_b32 s63, v50, s63
	s_lshl_b32 s63, s63, 10
	s_add_i32 s63, s63, s62
	s_nop 2
	buffer_load_dwordx4 v[50:53], v0, s[92:95], s63 offen
	v_mov_b32_e32 v97, v1
	v_mov_b32_e32 v98, v1
	s_waitcnt vmcnt(6)
	v_dot8c_i32_i4_e32 v97, v62, v74
	v_dot8c_i32_i4_e32 v98, v62, v70
	v_dot8c_i32_i4_e32 v97, v63, v75
	v_dot8c_i32_i4_e32 v98, v63, v71
	v_dot8c_i32_i4_e32 v97, v64, v76
	v_dot8c_i32_i4_e32 v98, v64, v72
	v_dot8c_i32_i4_e32 v97, v65, v77
	v_dot8c_i32_i4_e32 v98, v65, v73
	s_bitcmp0_b32 s57, 6
	s_cselect_b64 vcc, -1, 0
	s_nop 0
	v_lshl_add_u32 v62, v97, 4, v98
	v_cvt_f32_i32_e32 v97, v62
	v_cndmask_b32_e32 v62, v79, v78, vcc
	s_nop 0
	v_readlane_b32 s63, v62, s57
	s_lshl_b32 s63, s63, 10
	s_add_i32 s63, s63, s62
	s_nop 2
	buffer_load_dwordx4 v[62:65], v0, s[92:95], s63 offen
	v_cndmask_b32_e64 v98, v90, v69, s[0:1]
	v_cndmask_b32_e64 v69, v69, v90, s[0:1]
	v_cndmask_b32_e64 v90, v91, v83, s[0:1]
	v_cndmask_b32_e64 v83, v83, v91, s[0:1]
	v_cndmask_b32_e64 v91, v92, v84, s[0:1]
	v_cndmask_b32_e64 v84, v84, v92, s[0:1]
	v_cndmask_b32_e64 v92, v93, v85, s[0:1]
	v_cndmask_b32_e64 v85, v85, v93, s[0:1]
	v_cndmask_b32_e64 v93, v94, v86, s[0:1]
	v_cndmask_b32_e64 v86, v86, v94, s[0:1]
	v_cndmask_b32_e64 v94, v95, v87, s[0:1]
	v_cndmask_b32_e64 v87, v87, v95, s[0:1]
	v_cndmask_b32_e64 v95, v96, v88, s[0:1]
	v_cndmask_b32_e64 v88, v88, v96, s[0:1]
	v_cndmask_b32_e64 v96, v97, v89, s[0:1]
	v_cndmask_b32_e64 v89, v89, v97, s[0:1]
	ds_bpermute_b32 v69, v190, v69
	ds_bpermute_b32 v83, v190, v83
	ds_bpermute_b32 v84, v190, v84
	ds_bpermute_b32 v85, v190, v85
	ds_bpermute_b32 v86, v190, v86
	ds_bpermute_b32 v87, v190, v87
	ds_bpermute_b32 v88, v190, v88
	ds_bpermute_b32 v89, v190, v89
	s_waitcnt lgkmcnt(7)
; __device__ __forceinline__ int shl_i(int v, int from_lane) { return __builtin_amdgcn_ds_bpermute(from_lane << 2, v); }
; __device__ __forceinline__ void gather_sorted_ids(const int* IDX, const float* GWt, int t, int lane, int& id0, int& id1, float& g0, float& g1) {
;     const int ia = IDX[(size_t)t * 128 + lane], ib = IDX[(size_t)t * 128 + 64 + lane];
;     const float ga = GWt[(size_t)t * 128 + lane], gb = GWt[(size_t)t * 128 + 64 + lane];
;     ...
;         GATHER_U_SECTION(0, g0, w0)
;         GATHER_U_SECTION(1, g1, w1)
;         const float wm = wave_max(fmaxf(fabsf(w0), fabsf(w1)));
;         const float wsq = (wm > 0.f) ? 127.0f / wm : 0.f;
;         const int q0 = (int)rintf(w0 * wsq), q1 = (int)rintf(w1 * wsq);
;         const int c8 = 8 * (int)wave_sum((float)(q0 + q1));
;         const int pk0 = (q0 & 0xFF) | ((shl_i(q0, lane + 1) & 0xFF) << 8) | ((shl_i(q0, lane + 2) & 0xFF) << 16) | (shl_i(q0, lane + 3) << 24);
;         const int pk1 = (q1 & 0xFF) | ((shl_i(q1, lane + 1) & 0xFF) << 8) | ((shl_i(q1, lane + 2) & 0xFF) << 16) | (shl_i(q1, lane + 3) << 24);
;         int acci[32];
; #pragma unroll
;         for (int i = 0; i < 32; ++i) acci[i] = 0;
	v_add_f32_e32 v69, v98, v69
	s_waitcnt lgkmcnt(6)
	v_add_f32_e32 v83, v90, v83
	s_waitcnt lgkmcnt(5)
	v_add_f32_e32 v84, v91, v84
	s_waitcnt lgkmcnt(4)
	v_add_f32_e32 v85, v92, v85
	s_waitcnt lgkmcnt(3)
	v_add_f32_e32 v86, v93, v86
	s_waitcnt lgkmcnt(2)
	v_add_f32_e32 v87, v94, v87
	s_waitcnt lgkmcnt(1)
	v_add_f32_e32 v88, v95, v88
	s_waitcnt lgkmcnt(0)
	v_add_f32_e32 v89, v96, v89
	v_cndmask_b32_e64 v90, v86, v69, s[2:3]
	v_cndmask_b32_e64 v69, v69, v86, s[2:3]
	v_cndmask_b32_e64 v86, v87, v83, s[2:3]
	v_cndmask_b32_e64 v83, v83, v87, s[2:3]
	v_cndmask_b32_e64 v87, v88, v84, s[2:3]
	v_cndmask_b32_e64 v84, v84, v88, s[2:3]
	v_cndmask_b32_e64 v88, v89, v85, s[2:3]
	v_cndmask_b32_e64 v85, v85, v89, s[2:3]
	ds_bpermute_b32 v69, v189, v69
	ds_bpermute_b32 v83, v189, v83
	ds_bpermute_b32 v84, v189, v84
	ds_bpermute_b32 v85, v189, v85
	s_add_i32 s57, s57, 16
	s_waitcnt lgkmcnt(3)
	v_add_f32_e32 v69, v90, v69
	s_waitcnt lgkmcnt(2)
	v_add_f32_e32 v83, v86, v83
	s_waitcnt lgkmcnt(1)
	v_add_f32_e32 v84, v87, v84
	s_waitcnt lgkmcnt(0)
	v_add_f32_e32 v85, v88, v85
	v_cndmask_b32_e64 v86, v84, v69, s[4:5]
	v_cndmask_b32_e64 v69, v69, v84, s[4:5]
	v_cndmask_b32_e64 v84, v85, v83, s[4:5]
	v_cndmask_b32_e64 v83, v83, v85, s[4:5]
	ds_bpermute_b32 v69, v188, v69
	ds_bpermute_b32 v83, v188, v83
	s_waitcnt lgkmcnt(1)
	v_add_f32_e32 v69, v86, v69
	s_waitcnt lgkmcnt(0)
	v_add_f32_e32 v83, v84, v83
	v_cndmask_b32_e64 v84, v83, v69, s[6:7]
	v_cndmask_b32_e64 v69, v69, v83, s[6:7]
	ds_bpermute_b32 v69, v163, v69
	s_waitcnt lgkmcnt(0)
	v_add_f32_e32 v69, v84, v69
	v_mov_b32_e32 v83, v69
	s_nop 1
	v_permlane16_swap_b32_e32 v69, v83
	v_add_f32_e32 v69, v69, v83
	v_mov_b32_e32 v83, v69
	s_nop 1
	v_permlane32_swap_b32_e32 v69, v83
	v_add_f32_e32 v69, v69, v83
	v_mul_f32_e32 v69, v66, v69
	v_fma_f32 v83, |v69|, s66, 1.0
	v_rcp_f32_e32 v83, v83
	v_mul_f32_e32 v84, v69, v69
	v_mul_f32_e32 v84, 0xbf38aa3b, v84
	v_exp_f32_e32 v84, v84
	v_fmamk_f32 v85, v83, 0x3f07dc22, v207
	v_fmaak_f32 v85, v83, v85, 0x3f35f0e3
	v_fmaak_f32 v85, v83, v85, 0xbe11a98e
	v_fmaak_f32 v85, v83, v85, 0x3e027906
	v_mul_f32_e32 v83, v83, v85
	v_mul_f32_e32 v83, v84, v83
	v_mul_f32_e32 v84, v69, v83
	v_fma_f32 v83, -v69, v83, v69
	v_cmp_gt_f32_e32 vcc, 0, v69
	s_nop 1
	v_cndmask_b32_e32 v69, v83, v84, vcc
	v_mul_f32_e32 v69, 0x3d4ccccd, v69
	v_mul_f32_e32 v69, v80, v69
	v_cmp_eq_u32_e32 vcc, s56, v193
	s_add_i32 s56, s56, 1
	s_cmpk_eq_i32 s57, 0x9f
	v_cndmask_b32_e32 v82, v82, v69, vcc
	s_cbranch_scc0 .LBB0_1421
	v_max_f32_e64 v66, |v82|, |v82|
	v_max_f32_e64 v69, |v81|, |v81|
	v_max_f32_e32 v66, v69, v66
	v_mov_b32_e32 v69, 0
	s_mov_b32 s57, 0x42fe0000
	v_mbcnt_lo_u32_b32 v69, -1, v69
	v_mbcnt_hi_u32_b32 v69, -1, v69
	v_lshlrev_b32_e32 v71, 2, v69
	v_xor_b32_e32 v69, 0x80, v71
	ds_bpermute_b32 v69, v69, v66
	v_xor_b32_e32 v70, 64, v71
	v_xor_b32_e32 v72, 8, v71
	v_mov_b32_e32 v83, 0
	s_waitcnt lgkmcnt(0)
	v_max_f32_e32 v69, v69, v69
	v_max_f32_e32 v66, v66, v69
	ds_bpermute_b32 v69, v70, v66
	v_xor_b32_e32 v70, 32, v71
	s_movk_i32 s56, 0x9f
	v_mov_b32_e32 v74, 0
	v_mov_b32_e32 v75, 0
	s_waitcnt lgkmcnt(0)
	v_max_f32_e32 v69, v69, v69
	v_max_f32_e32 v66, v66, v69
	ds_bpermute_b32 v69, v70, v66
	v_xor_b32_e32 v70, 16, v71
	v_xor_b32_e32 v71, 4, v71
	v_mov_b32_e32 v76, 0
	v_mov_b32_e32 v80, 0
	s_waitcnt lgkmcnt(0)
	v_max_f32_e32 v69, v69, v69
	v_max_f32_e32 v69, v66, v69
	ds_bpermute_b32 v70, v70, v69
	v_mov_b32_e32 v66, 0
	v_mov_b32_e32 v94, 0
	v_mov_b32_e32 v95, 0
	v_mov_b32_e32 v96, 0
	s_waitcnt lgkmcnt(0)
	v_max_f32_e32 v70, v70, v70
	v_max_f32_e32 v73, v69, v70
	ds_bpermute_b32 v72, v72, v73
	v_mov_b32_e32 v69, 0
	v_mov_b32_e32 v70, 0
	v_mov_b32_e32 v97, 0
	v_mov_b32_e32 v98, 0
	s_waitcnt lgkmcnt(0)
	v_max_f32_e32 v72, v72, v72
	v_max_f32_e32 v77, v73, v72
	ds_bpermute_b32 v71, v71, v77
	v_mov_b32_e32 v72, 0
	v_mov_b32_e32 v73, 0
	v_mov_b32_e32 v99, 0
	v_mov_b32_e32 v100, 0
	s_waitcnt lgkmcnt(0)
	v_max_f32_e32 v71, v71, v71
	v_max_f32_e32 v71, v77, v71
	v_div_scale_f32 v77, s[62:63], v71, v71, s57
	v_rcp_f32_e32 v84, v77
	v_div_scale_f32 v85, vcc, s57, v71, s57
	v_mov_b32_e32 v101, 0
	v_fma_f32 v86, -v77, v84, 1.0
	v_fmac_f32_e32 v84, v86, v84
	v_mul_f32_e32 v86, v85, v84
	v_fma_f32 v87, -v77, v86, v85
	v_fmac_f32_e32 v86, v87, v84
	v_fma_f32 v77, -v77, v86, v85
	v_div_fmas_f32 v77, v77, v84, v86
	v_div_fixup_f32 v77, v77, v71, s57
	v_cmp_lt_f32_e32 vcc, 0, v71
	s_mov_b32 s57, 0xc0c0500
	v_mov_b32_e32 v85, 0
	v_cndmask_b32_e32 v77, 0, v77, vcc
	v_mul_f32_e32 v81, v81, v77
	v_mul_f32_e32 v77, v82, v77
	v_rndne_f32_e32 v81, v81
	v_rndne_f32_e32 v77, v77
	v_cvt_i32_f32_e32 v82, v81
	v_cvt_i32_f32_e32 v107, v77
	v_mbcnt_lo_u32_b32 v81, -1, v83
	v_mbcnt_hi_u32_b32 v81, -1, v81
	v_lshlrev_b32_e32 v84, 2, v81
	v_add_u32_e32 v83, v82, v107
	v_cvt_f32_i32_e32 v83, v83
	v_xor_b32_e32 v81, 0x80, v84
	v_xor_b32_e32 v88, 64, v84
	v_xor_b32_e32 v89, 16, v84
	ds_bpermute_b32 v87, v81, v83
	v_xor_b32_e32 v90, 8, v84
	ds_bpermute_b32 v91, v195, v82
	ds_bpermute_b32 v92, v196, v82
	ds_bpermute_b32 v108, v194, v107
	s_waitcnt lgkmcnt(3)
	v_add_f32_e32 v83, v87, v83
	ds_bpermute_b32 v87, v88, v83
	v_xor_b32_e32 v88, 32, v84
	v_xor_b32_e32 v84, 4, v84
	ds_bpermute_b32 v109, v195, v107
	ds_bpermute_b32 v110, v196, v107
	s_waitcnt lgkmcnt(2)
	v_add_f32_e32 v83, v83, v87
	ds_bpermute_b32 v87, v88, v83
	ds_bpermute_b32 v88, v194, v82
	v_mov_b32_e32 v77, 0
	v_mov_b32_e32 v81, 0
	v_mov_b32_e32 v86, 0
	s_waitcnt lgkmcnt(1)
	v_add_f32_e32 v83, v83, v87
	ds_bpermute_b32 v87, v89, v83
	s_waitcnt lgkmcnt(1)
	v_lshlrev_b32_e32 v88, 8, v88
	v_lshlrev_b32_e32 v89, 16, v91
	v_perm_b32 v82, v88, v82, s57
	v_and_b32_e32 v88, 0xff0000, v89
	s_waitcnt lgkmcnt(0)
	v_add_f32_e32 v83, v83, v87
	ds_bpermute_b32 v87, v90, v83
	v_lshlrev_b32_e32 v90, 24, v92
	v_or3_b32 v111, v82, v88, v90
	v_mov_b32_e32 v82, 0
	v_mov_b32_e32 v88, 0
	s_waitcnt lgkmcnt(0)
	v_add_f32_e32 v103, v83, v87
	ds_bpermute_b32 v104, v84, v103
	v_mov_b32_e32 v84, 0
	v_mov_b32_e32 v87, 0
	v_mov_b32_e32 v89, 0
	v_mov_b32_e32 v90, 0
	v_mov_b32_e32 v91, 0
	v_mov_b32_e32 v92, 0
	v_mov_b32_e32 v93, 0
	v_mov_b32_e32 v102, 0
	v_mov_b32_e32 v83, 0
	v_readlane_b32 s98, v254, 58
	v_readlane_b32 s99, v255, 1
	s_add_i32 s99, s98, s99
	s_cmp_lt_i32 s98, 0x4000
	s_cselect_b32 s98, s98, s88
	s_cmp_lt_i32 s99, 0x4000
	s_cselect_b32 s99, s99, s98
	s_lshl_b32 s99, s99, 9
	v_lshl_add_u32 v249, v130, 2, s99
	global_load_dword v245, v249, s[70:71] offset:256
	global_load_dword v246, v249, s[40:41] offset:256
	global_load_dword v247, v249, s[40:41]
	global_load_dword v248, v249, s[70:71]
	s_cmp_eq_u32 s101, 0
	s_cbranch_scc1 .Lnb_1423
	s_barrier

.Lnb_1425:
.LBB0_1425:
	s_add_i32 s56, s63, 0xffffff21
	s_waitcnt vmcnt(5)
	v_perm_b32 v106, v14, v6, s67
	v_perm_b32 v6, v14, v6, s68
	s_waitcnt vmcnt(3)
	v_perm_b32 v14, v46, v30, s67
	v_readlane_b32 s56, v105, s56
	v_perm_b32 v30, v46, v30, s68
	v_perm_b32 v46, v14, v106, s69
	v_perm_b32 v14, v14, v106, s33
	v_perm_b32 v106, v30, v6, s69
	v_perm_b32 v6, v30, v6, s33
	v_dot4c_i32_i8_e32 v74, s56, v14
	v_and_b32_e32 v14, 0xf0f0f0f0, v14
	v_dot4c_i32_i8_e32 v70, s56, v14
	v_and_b32_e32 v14, 0xf0f0f0f0, v106
	v_dot4c_i32_i8_e32 v76, s56, v6
	v_and_b32_e32 v6, 0xf0f0f0f0, v6
	v_and_b32_e32 v30, 0xf0f0f0f0, v46
	v_dot4c_i32_i8_e32 v72, s56, v14
	v_dot4c_i32_i8_e32 v73, s56, v6
	v_perm_b32 v6, v15, v7, s67
	v_perm_b32 v14, v47, v31, s67
	v_dot4c_i32_i8_e32 v69, s56, v30
	v_perm_b32 v7, v15, v7, s68
	v_perm_b32 v15, v47, v31, s68
	v_perm_b32 v30, v14, v6, s69
	v_perm_b32 v6, v14, v6, s33
	v_perm_b32 v14, v15, v7, s69
	v_dot4c_i32_i8_e32 v85, s56, v6
	v_and_b32_e32 v6, 0xf0f0f0f0, v6
	v_perm_b32 v7, v15, v7, s33
	v_dot4c_i32_i8_e32 v81, s56, v6
	v_and_b32_e32 v6, 0xf0f0f0f0, v14
	v_dot4c_i32_i8_e32 v82, s56, v6
	v_and_b32_e32 v6, 0xf0f0f0f0, v7
	v_and_b32_e32 v15, 0xf0f0f0f0, v30
	v_dot4c_i32_i8_e32 v94, s56, v7
	v_dot4c_i32_i8_e32 v84, s56, v6
	v_perm_b32 v6, v16, v8, s67
	v_perm_b32 v7, v16, v8, s68
	v_perm_b32 v8, v48, v32, s67
	v_dot4c_i32_i8_e32 v77, s56, v15
	v_dot4c_i32_i8_e32 v86, s56, v14
	v_perm_b32 v14, v48, v32, s68
	v_perm_b32 v15, v8, v6, s69
	v_perm_b32 v6, v8, v6, s33
	v_perm_b32 v8, v14, v7, s69
	v_dot4c_i32_i8_e32 v96, s56, v6
	v_and_b32_e32 v6, 0xf0f0f0f0, v6
	v_perm_b32 v7, v14, v7, s33
	v_dot4c_i32_i8_e32 v88, s56, v6
	v_and_b32_e32 v6, 0xf0f0f0f0, v8
	v_dot4c_i32_i8_e32 v89, s56, v6
	v_and_b32_e32 v6, 0xf0f0f0f0, v7
	v_and_b32_e32 v14, 0xf0f0f0f0, v15
	v_dot4c_i32_i8_e32 v97, s56, v8
	v_dot4c_i32_i8_e32 v90, s56, v6
	v_perm_b32 v6, v17, v9, s67
	v_perm_b32 v8, v49, v33, s67
	v_dot4c_i32_i8_e32 v87, s56, v14
	v_dot4c_i32_i8_e32 v98, s56, v7
	v_perm_b32 v7, v17, v9, s68
	v_perm_b32 v9, v49, v33, s68
	v_perm_b32 v14, v8, v6, s69
	v_perm_b32 v6, v8, v6, s33
	v_perm_b32 v8, v9, v7, s69
	v_dot4c_i32_i8_e32 v100, s56, v6
	v_and_b32_e32 v6, 0xf0f0f0f0, v6
	s_add_i32 s91, s63, -15
	v_perm_b32 v7, v9, v7, s33
	v_dot4c_i32_i8_e32 v92, s56, v6
	v_and_b32_e32 v6, 0xf0f0f0f0, v8
	s_cmp_gt_u32 s62, 2
	v_and_b32_e32 v9, 0xf0f0f0f0, v14
	v_dot4c_i32_i8_e32 v93, s56, v6
	v_and_b32_e32 v6, 0xf0f0f0f0, v7
	s_cselect_b64 vcc, -1, 0
	s_bitcmp0_b32 s91, 6
	v_dot4c_i32_i8_e32 v66, s56, v46
	v_dot4c_i32_i8_e32 v75, s56, v106
	v_dot4c_i32_i8_e32 v80, s56, v30
	v_dot4c_i32_i8_e32 v95, s56, v15
	v_dot4c_i32_i8_e32 v99, s56, v14
	v_dot4c_i32_i8_e32 v91, s56, v9
	v_dot4c_i32_i8_e32 v101, s56, v8
	v_dot4c_i32_i8_e32 v102, s56, v7
	v_dot4c_i32_i8_e32 v83, s56, v6
	s_cselect_b64 s[56:57], -1, 0
	v_cndmask_b32_e64 v6, v79, v78, s[56:57]
	v_cndmask_b32_e32 v6, v6, v199, vcc
	s_add_i32 s57, s90, 0xffe20000
	v_readlane_b32 s56, v6, s91
	s_lshl_b32 s56, s56, 10
	s_and_b32 s57, s57, 0x1000000
	s_add_i32 s56, s56, s57
	s_add_i32 s91, s63, -14
	s_bitcmp0_b32 s91, 6
	buffer_load_dwordx4 v[6:9], v0, s[92:95], s56 offen
	s_cselect_b64 s[56:57], -1, 0
	v_cndmask_b32_e64 v14, v79, v78, s[56:57]
	v_cndmask_b32_e32 v14, v14, v199, vcc
	s_add_i32 s57, s90, 0xffe40000
	v_readlane_b32 s56, v14, s91
	s_lshl_b32 s56, s56, 10
	s_and_b32 s57, s57, 0x1000000
	s_add_i32 s56, s56, s57
	s_add_i32 s91, s63, -13
	s_bitcmp0_b32 s91, 6
	buffer_load_dwordx4 v[14:17], v0, s[92:95], s56 offen
	s_cselect_b64 s[56:57], -1, 0
	v_cndmask_b32_e64 v30, v79, v78, s[56:57]
	v_cndmask_b32_e32 v30, v30, v199, vcc
	s_add_i32 s57, s90, 0xffe60000
	v_readlane_b32 s56, v30, s91
	s_lshl_b32 s56, s56, 10
	s_and_b32 s57, s57, 0x1000000
	s_add_i32 s56, s56, s57
	s_add_i32 s91, s63, -12
	s_bitcmp0_b32 s91, 6
	buffer_load_dwordx4 v[30:33], v0, s[92:95], s56 offen
	s_cselect_b64 s[56:57], -1, 0
	v_cndmask_b32_e64 v46, v79, v78, s[56:57]
	v_cndmask_b32_e32 v46, v46, v199, vcc
	s_add_i32 s57, s90, 0xffe80000
	v_readlane_b32 s56, v46, s91
	s_lshl_b32 s56, s56, 10
	s_and_b32 s57, s57, 0x1000000
	s_add_i32 s56, s56, s57
	s_nop 1
	buffer_load_dwordx4 v[46:49], v0, s[92:95], s56 offen
	s_add_i32 s56, s63, 0xffffff25
	s_waitcnt vmcnt(5)
	v_perm_b32 v106, v22, v2, s67
	v_perm_b32 v2, v22, v2, s68
	s_waitcnt vmcnt(3)
	v_perm_b32 v22, v54, v38, s67
	v_readlane_b32 s56, v105, s56
	v_perm_b32 v38, v54, v38, s68
	v_perm_b32 v54, v22, v106, s69
	v_perm_b32 v22, v22, v106, s33
	v_perm_b32 v106, v38, v2, s69
	v_perm_b32 v2, v38, v2, s33
	v_dot4c_i32_i8_e32 v74, s56, v22
	v_and_b32_e32 v22, 0xf0f0f0f0, v22
	v_dot4c_i32_i8_e32 v70, s56, v22
	v_and_b32_e32 v22, 0xf0f0f0f0, v106
	v_dot4c_i32_i8_e32 v76, s56, v2
	v_and_b32_e32 v2, 0xf0f0f0f0, v2
	v_and_b32_e32 v38, 0xf0f0f0f0, v54
	v_dot4c_i32_i8_e32 v72, s56, v22
	v_dot4c_i32_i8_e32 v73, s56, v2
	v_perm_b32 v2, v23, v3, s67
	v_perm_b32 v22, v55, v39, s67
	v_dot4c_i32_i8_e32 v69, s56, v38
	v_perm_b32 v3, v23, v3, s68
	v_perm_b32 v23, v55, v39, s68
	v_perm_b32 v38, v22, v2, s69
	v_perm_b32 v2, v22, v2, s33
	v_perm_b32 v22, v23, v3, s69
	v_dot4c_i32_i8_e32 v85, s56, v2
	v_and_b32_e32 v2, 0xf0f0f0f0, v2
	v_perm_b32 v3, v23, v3, s33
	v_dot4c_i32_i8_e32 v81, s56, v2
	v_and_b32_e32 v2, 0xf0f0f0f0, v22
	v_dot4c_i32_i8_e32 v82, s56, v2
	v_and_b32_e32 v2, 0xf0f0f0f0, v3
	v_and_b32_e32 v23, 0xf0f0f0f0, v38
	v_dot4c_i32_i8_e32 v94, s56, v3
	v_dot4c_i32_i8_e32 v84, s56, v2
	v_perm_b32 v2, v24, v4, s67
	v_perm_b32 v3, v24, v4, s68
	v_perm_b32 v4, v56, v40, s67
	v_dot4c_i32_i8_e32 v77, s56, v23
	v_dot4c_i32_i8_e32 v86, s56, v22
	v_perm_b32 v22, v56, v40, s68
	v_perm_b32 v23, v4, v2, s69
	v_perm_b32 v2, v4, v2, s33
	v_perm_b32 v4, v22, v3, s69
	v_dot4c_i32_i8_e32 v96, s56, v2
	v_and_b32_e32 v2, 0xf0f0f0f0, v2
	v_perm_b32 v3, v22, v3, s33
	v_dot4c_i32_i8_e32 v88, s56, v2
	v_and_b32_e32 v2, 0xf0f0f0f0, v4
	v_dot4c_i32_i8_e32 v89, s56, v2
	v_and_b32_e32 v2, 0xf0f0f0f0, v3
	v_and_b32_e32 v22, 0xf0f0f0f0, v23
	v_dot4c_i32_i8_e32 v97, s56, v4
	v_dot4c_i32_i8_e32 v90, s56, v2
	v_perm_b32 v2, v25, v5, s67
	v_perm_b32 v4, v57, v41, s67
	v_dot4c_i32_i8_e32 v87, s56, v22
	v_dot4c_i32_i8_e32 v98, s56, v3
	v_perm_b32 v3, v25, v5, s68
	v_perm_b32 v5, v57, v41, s68
	v_perm_b32 v22, v4, v2, s69
	v_perm_b32 v2, v4, v2, s33
	v_perm_b32 v4, v5, v3, s69
	v_dot4c_i32_i8_e32 v100, s56, v2
	v_and_b32_e32 v2, 0xf0f0f0f0, v2
	v_perm_b32 v3, v5, v3, s33
	v_dot4c_i32_i8_e32 v92, s56, v2
	v_and_b32_e32 v2, 0xf0f0f0f0, v4
	s_add_i32 s91, s63, -11
	v_and_b32_e32 v5, 0xf0f0f0f0, v22
	v_dot4c_i32_i8_e32 v93, s56, v2
	v_and_b32_e32 v2, 0xf0f0f0f0, v3
	s_bitcmp0_b32 s91, 6
	v_dot4c_i32_i8_e32 v66, s56, v54
	v_dot4c_i32_i8_e32 v75, s56, v106
	v_dot4c_i32_i8_e32 v80, s56, v38
	v_dot4c_i32_i8_e32 v95, s56, v23
	v_dot4c_i32_i8_e32 v99, s56, v22
	v_dot4c_i32_i8_e32 v91, s56, v5
	v_dot4c_i32_i8_e32 v101, s56, v4
	v_dot4c_i32_i8_e32 v102, s56, v3
	v_dot4c_i32_i8_e32 v83, s56, v2
	s_cselect_b64 s[56:57], -1, 0
	v_cndmask_b32_e64 v2, v79, v78, s[56:57]
	v_cndmask_b32_e32 v2, v2, v199, vcc
	s_add_i32 s57, s90, 0xffea0000
	v_readlane_b32 s56, v2, s91
	s_lshl_b32 s56, s56, 10
	s_and_b32 s57, s57, 0x1000000
	s_add_i32 s56, s56, s57
	s_add_i32 s91, s63, -10
	s_bitcmp0_b32 s91, 6
	buffer_load_dwordx4 v[2:5], v0, s[92:95], s56 offen
	s_cselect_b64 s[56:57], -1, 0
	v_cndmask_b32_e64 v22, v79, v78, s[56:57]
	v_cndmask_b32_e32 v22, v22, v199, vcc
	s_add_i32 s57, s90, 0xffec0000
	v_readlane_b32 s56, v22, s91
	s_lshl_b32 s56, s56, 10
	s_and_b32 s57, s57, 0x1000000
	s_add_i32 s56, s56, s57
	s_add_i32 s91, s63, -9
	s_bitcmp0_b32 s91, 6
	buffer_load_dwordx4 v[22:25], v0, s[92:95], s56 offen
	s_cselect_b64 s[56:57], -1, 0
	v_cndmask_b32_e64 v38, v79, v78, s[56:57]
	v_cndmask_b32_e32 v38, v38, v199, vcc
	s_add_i32 s57, s90, 0xffee0000
	v_readlane_b32 s56, v38, s91
	s_lshl_b32 s56, s56, 10
	s_and_b32 s57, s57, 0x1000000
	s_add_i32 s56, s56, s57
	s_add_i32 s91, s63, -8
	s_bitcmp0_b32 s91, 6
	buffer_load_dwordx4 v[38:41], v0, s[92:95], s56 offen
	s_cselect_b64 s[56:57], -1, 0
	v_cndmask_b32_e64 v54, v79, v78, s[56:57]
	v_cndmask_b32_e32 v54, v54, v199, vcc
	s_add_i32 s57, s90, 0xfff00000
	v_readlane_b32 s56, v54, s91
	s_lshl_b32 s56, s56, 10
	s_and_b32 s57, s57, 0x1000000
	s_add_i32 s56, s56, s57
	s_nop 1
	buffer_load_dwordx4 v[54:57], v0, s[92:95], s56 offen
	s_add_i32 s56, s63, 0xffffff29
	s_waitcnt vmcnt(5)
	v_perm_b32 v106, v26, v10, s67
	v_perm_b32 v10, v26, v10, s68
	s_waitcnt vmcnt(3)
	v_perm_b32 v26, v58, v42, s67
	v_readlane_b32 s56, v105, s56
	v_perm_b32 v42, v58, v42, s68
	v_perm_b32 v58, v26, v106, s69
	v_perm_b32 v26, v26, v106, s33
	v_perm_b32 v106, v42, v10, s69
	v_perm_b32 v10, v42, v10, s33
	v_dot4c_i32_i8_e32 v74, s56, v26
	v_and_b32_e32 v26, 0xf0f0f0f0, v26
	v_dot4c_i32_i8_e32 v70, s56, v26
	v_and_b32_e32 v26, 0xf0f0f0f0, v106
	v_dot4c_i32_i8_e32 v76, s56, v10
	v_and_b32_e32 v10, 0xf0f0f0f0, v10
	v_and_b32_e32 v42, 0xf0f0f0f0, v58
	v_dot4c_i32_i8_e32 v72, s56, v26
	v_dot4c_i32_i8_e32 v73, s56, v10
	v_perm_b32 v10, v27, v11, s67
	v_perm_b32 v26, v59, v43, s67
	v_dot4c_i32_i8_e32 v69, s56, v42
	v_perm_b32 v11, v27, v11, s68
	v_perm_b32 v27, v59, v43, s68
	v_perm_b32 v42, v26, v10, s69
	v_perm_b32 v10, v26, v10, s33
	v_perm_b32 v26, v27, v11, s69
	v_dot4c_i32_i8_e32 v85, s56, v10
	v_and_b32_e32 v10, 0xf0f0f0f0, v10
	v_perm_b32 v11, v27, v11, s33
	v_dot4c_i32_i8_e32 v81, s56, v10
	v_and_b32_e32 v10, 0xf0f0f0f0, v26
	v_dot4c_i32_i8_e32 v82, s56, v10
	v_and_b32_e32 v10, 0xf0f0f0f0, v11
	v_and_b32_e32 v27, 0xf0f0f0f0, v42
	v_dot4c_i32_i8_e32 v94, s56, v11
	v_dot4c_i32_i8_e32 v84, s56, v10
	v_perm_b32 v10, v28, v12, s67
	v_perm_b32 v11, v28, v12, s68
	v_perm_b32 v12, v60, v44, s67
	v_dot4c_i32_i8_e32 v77, s56, v27
	v_dot4c_i32_i8_e32 v86, s56, v26
	v_perm_b32 v26, v60, v44, s68
	v_perm_b32 v27, v12, v10, s69
	v_perm_b32 v10, v12, v10, s33
	v_perm_b32 v12, v26, v11, s69
	v_dot4c_i32_i8_e32 v96, s56, v10
	v_and_b32_e32 v10, 0xf0f0f0f0, v10
	v_perm_b32 v11, v26, v11, s33
	v_dot4c_i32_i8_e32 v88, s56, v10
	v_and_b32_e32 v10, 0xf0f0f0f0, v12
	v_dot4c_i32_i8_e32 v89, s56, v10
	v_and_b32_e32 v10, 0xf0f0f0f0, v11
	v_and_b32_e32 v26, 0xf0f0f0f0, v27
	v_dot4c_i32_i8_e32 v97, s56, v12
	v_dot4c_i32_i8_e32 v90, s56, v10
	v_perm_b32 v10, v29, v13, s67
	v_perm_b32 v12, v61, v45, s67
	v_dot4c_i32_i8_e32 v87, s56, v26
	v_dot4c_i32_i8_e32 v98, s56, v11
	v_perm_b32 v11, v29, v13, s68
	v_perm_b32 v13, v61, v45, s68
	v_perm_b32 v26, v12, v10, s69
	v_perm_b32 v10, v12, v10, s33
	v_perm_b32 v12, v13, v11, s69
	v_dot4c_i32_i8_e32 v100, s56, v10
	v_and_b32_e32 v10, 0xf0f0f0f0, v10
	v_perm_b32 v11, v13, v11, s33
	v_dot4c_i32_i8_e32 v92, s56, v10
	v_and_b32_e32 v10, 0xf0f0f0f0, v12
	s_add_i32 s91, s63, -7
	v_and_b32_e32 v13, 0xf0f0f0f0, v26
	v_dot4c_i32_i8_e32 v93, s56, v10
	v_and_b32_e32 v10, 0xf0f0f0f0, v11
	s_bitcmp0_b32 s91, 6
	v_dot4c_i32_i8_e32 v66, s56, v58
	v_dot4c_i32_i8_e32 v75, s56, v106
	v_dot4c_i32_i8_e32 v80, s56, v42
	v_dot4c_i32_i8_e32 v95, s56, v27
	v_dot4c_i32_i8_e32 v99, s56, v26
	v_dot4c_i32_i8_e32 v91, s56, v13
	v_dot4c_i32_i8_e32 v101, s56, v12
	v_dot4c_i32_i8_e32 v102, s56, v11
	v_dot4c_i32_i8_e32 v83, s56, v10
	s_cselect_b64 s[56:57], -1, 0
	v_cndmask_b32_e64 v10, v79, v78, s[56:57]
	v_cndmask_b32_e32 v10, v10, v199, vcc
	s_add_i32 s57, s90, 0xfff20000
	v_readlane_b32 s56, v10, s91
	s_lshl_b32 s56, s56, 10
	s_and_b32 s57, s57, 0x1000000
	s_add_i32 s56, s56, s57
	s_add_i32 s91, s63, -6
	s_bitcmp0_b32 s91, 6
	buffer_load_dwordx4 v[10:13], v0, s[92:95], s56 offen
	s_cselect_b64 s[56:57], -1, 0
	v_cndmask_b32_e64 v26, v79, v78, s[56:57]
	v_cndmask_b32_e32 v26, v26, v199, vcc
	s_add_i32 s57, s90, 0xfff40000
	v_readlane_b32 s56, v26, s91
	s_lshl_b32 s56, s56, 10
	s_and_b32 s57, s57, 0x1000000
	s_add_i32 s56, s56, s57
	s_add_i32 s91, s63, -5
	s_bitcmp0_b32 s91, 6
	buffer_load_dwordx4 v[26:29], v0, s[92:95], s56 offen
	s_cselect_b64 s[56:57], -1, 0
	v_cndmask_b32_e64 v42, v79, v78, s[56:57]
	v_cndmask_b32_e32 v42, v42, v199, vcc
	s_add_i32 s57, s90, 0xfff60000
	v_readlane_b32 s56, v42, s91
	s_lshl_b32 s56, s56, 10
	s_and_b32 s57, s57, 0x1000000
	s_add_i32 s56, s56, s57
	s_add_i32 s91, s63, -4
	s_bitcmp0_b32 s91, 6
	buffer_load_dwordx4 v[42:45], v0, s[92:95], s56 offen
	s_cselect_b64 s[56:57], -1, 0
	v_cndmask_b32_e64 v58, v79, v78, s[56:57]
	v_cndmask_b32_e32 v58, v58, v199, vcc
	s_add_i32 s57, s90, 0xfff80000
	v_readlane_b32 s56, v58, s91
	s_lshl_b32 s56, s56, 10
	s_and_b32 s57, s57, 0x1000000
	s_add_i32 s56, s56, s57
	s_nop 1
	buffer_load_dwordx4 v[58:61], v0, s[92:95], s56 offen
	s_add_i32 s56, s63, 0xffffff2d
	s_waitcnt vmcnt(5)
	v_perm_b32 v106, v34, v18, s67
	v_perm_b32 v18, v34, v18, s68
	s_waitcnt vmcnt(3)
	v_perm_b32 v34, v62, v50, s67
	v_readlane_b32 s56, v105, s56
	v_perm_b32 v50, v62, v50, s68
	v_perm_b32 v62, v34, v106, s69
	v_perm_b32 v34, v34, v106, s33
	v_perm_b32 v106, v50, v18, s69
	v_perm_b32 v18, v50, v18, s33
	v_dot4c_i32_i8_e32 v74, s56, v34
	v_and_b32_e32 v34, 0xf0f0f0f0, v34
	v_dot4c_i32_i8_e32 v70, s56, v34
	v_and_b32_e32 v34, 0xf0f0f0f0, v106
	v_dot4c_i32_i8_e32 v76, s56, v18
	v_and_b32_e32 v18, 0xf0f0f0f0, v18
	v_and_b32_e32 v50, 0xf0f0f0f0, v62
	v_dot4c_i32_i8_e32 v72, s56, v34
	v_dot4c_i32_i8_e32 v73, s56, v18
	v_perm_b32 v18, v35, v19, s67
	v_perm_b32 v34, v63, v51, s67
	v_dot4c_i32_i8_e32 v69, s56, v50
	v_perm_b32 v19, v35, v19, s68
	v_perm_b32 v35, v63, v51, s68
	v_perm_b32 v50, v34, v18, s69
	v_perm_b32 v18, v34, v18, s33
	v_perm_b32 v34, v35, v19, s69
	v_dot4c_i32_i8_e32 v85, s56, v18
	v_and_b32_e32 v18, 0xf0f0f0f0, v18
	v_perm_b32 v19, v35, v19, s33
	v_dot4c_i32_i8_e32 v81, s56, v18
	v_and_b32_e32 v18, 0xf0f0f0f0, v34
	v_dot4c_i32_i8_e32 v82, s56, v18
	v_and_b32_e32 v18, 0xf0f0f0f0, v19
	v_and_b32_e32 v35, 0xf0f0f0f0, v50
	v_dot4c_i32_i8_e32 v94, s56, v19
	v_dot4c_i32_i8_e32 v84, s56, v18
	v_perm_b32 v18, v36, v20, s67
	v_perm_b32 v19, v36, v20, s68
	v_perm_b32 v20, v64, v52, s67
	v_dot4c_i32_i8_e32 v77, s56, v35
	v_dot4c_i32_i8_e32 v86, s56, v34
	v_perm_b32 v34, v64, v52, s68
	v_perm_b32 v35, v20, v18, s69
	v_perm_b32 v18, v20, v18, s33
	v_perm_b32 v20, v34, v19, s69
	v_dot4c_i32_i8_e32 v96, s56, v18
	v_and_b32_e32 v18, 0xf0f0f0f0, v18
	v_perm_b32 v19, v34, v19, s33
	v_dot4c_i32_i8_e32 v88, s56, v18
	v_and_b32_e32 v18, 0xf0f0f0f0, v20
	v_dot4c_i32_i8_e32 v89, s56, v18
	v_and_b32_e32 v18, 0xf0f0f0f0, v19
	v_and_b32_e32 v34, 0xf0f0f0f0, v35
	v_dot4c_i32_i8_e32 v97, s56, v20
	v_dot4c_i32_i8_e32 v90, s56, v18
	v_perm_b32 v18, v37, v21, s67
	v_perm_b32 v20, v65, v53, s67
	v_dot4c_i32_i8_e32 v87, s56, v34
	v_dot4c_i32_i8_e32 v98, s56, v19
	v_perm_b32 v19, v37, v21, s68
	v_perm_b32 v21, v65, v53, s68
	v_perm_b32 v34, v20, v18, s69
	v_perm_b32 v18, v20, v18, s33
	v_perm_b32 v20, v21, v19, s69
	v_dot4c_i32_i8_e32 v100, s56, v18
	v_and_b32_e32 v18, 0xf0f0f0f0, v18
	v_perm_b32 v19, v21, v19, s33
	v_dot4c_i32_i8_e32 v92, s56, v18
	v_and_b32_e32 v18, 0xf0f0f0f0, v20
	s_add_i32 s91, s63, -3
	v_and_b32_e32 v21, 0xf0f0f0f0, v34
	v_dot4c_i32_i8_e32 v93, s56, v18
	v_and_b32_e32 v18, 0xf0f0f0f0, v19
	s_bitcmp0_b32 s91, 6
	v_dot4c_i32_i8_e32 v66, s56, v62
	v_dot4c_i32_i8_e32 v75, s56, v106
	v_dot4c_i32_i8_e32 v80, s56, v50
	v_dot4c_i32_i8_e32 v95, s56, v35
	v_dot4c_i32_i8_e32 v99, s56, v34
	v_dot4c_i32_i8_e32 v91, s56, v21
	v_dot4c_i32_i8_e32 v101, s56, v20
	v_dot4c_i32_i8_e32 v102, s56, v19
	v_dot4c_i32_i8_e32 v83, s56, v18
	s_cselect_b64 s[56:57], -1, 0
	v_cndmask_b32_e64 v18, v79, v78, s[56:57]
	v_cndmask_b32_e32 v18, v18, v199, vcc
	s_add_i32 s57, s90, 0xfffa0000
	v_readlane_b32 s56, v18, s91
	s_lshl_b32 s56, s56, 10
	s_and_b32 s57, s57, 0x1000000
	s_add_i32 s56, s56, s57
	s_add_i32 s91, s63, -2
	s_bitcmp0_b32 s91, 6
	buffer_load_dwordx4 v[18:21], v0, s[92:95], s56 offen
	s_cselect_b64 s[56:57], -1, 0
	v_cndmask_b32_e64 v34, v79, v78, s[56:57]
	v_cndmask_b32_e32 v34, v34, v199, vcc
	s_add_i32 s57, s90, 0xfffc0000
	v_readlane_b32 s56, v34, s91
	s_lshl_b32 s56, s56, 10
	s_and_b32 s57, s57, 0x1000000
	s_add_i32 s56, s56, s57
	s_add_i32 s91, s63, -1
	s_bitcmp0_b32 s91, 6
	buffer_load_dwordx4 v[34:37], v0, s[92:95], s56 offen
	s_cselect_b64 s[56:57], -1, 0
	v_cndmask_b32_e64 v50, v79, v78, s[56:57]
	v_cndmask_b32_e32 v50, v50, v199, vcc
	s_add_i32 s57, s90, 0xfffe0000
	v_readlane_b32 s56, v50, s91
	s_lshl_b32 s56, s56, 10
	s_and_b32 s57, s57, 0x1000000
	s_add_i32 s56, s56, s57
	s_bitcmp0_b32 s63, 6
	s_nop 0
	buffer_load_dwordx4 v[50:53], v0, s[92:95], s56 offen
	s_cselect_b64 s[56:57], -1, 0
	v_cndmask_b32_e64 v62, v79, v78, s[56:57]
	v_cndmask_b32_e32 v62, v62, v199, vcc
	s_and_b32 s57, s90, 0x1000000
	v_readlane_b32 s56, v62, s63
	s_lshl_b32 s56, s56, 10
	s_add_i32 s56, s56, s57
	s_nop 2
	buffer_load_dwordx4 v[62:65], v0, s[92:95], s56 offen
	s_add_i32 s62, s62, 1
	s_add_i32 s63, s63, 16
	s_add_i32 s90, s90, 0x200000
	s_cmpk_eq_i32 s63, 0x11f
	s_cbranch_scc0 .LBB0_1425
; __device__ __forceinline__ int ov(int x) { asm volatile("" : "+v"(x)); return x; }
;     ...
;         f32x2 acc[16];
;         { const float fsc = wm * (1.0f / 127.0f);
; #pragma unroll
;           for (int i = 0; i < 16; ++i) acc[i] = (f32x2){(float)(acci[2 * i] - acci[2 * i + 1] - c8) * fsc, (float)acci[2 * i + 1] * (fsc * 0.0625f)}; }
;         const int lane2 = ov(lane);
;         float s = 0.f;
; #pragma unroll
;         for (int hh = 0; hh < 4; ++hh) { float pl[8]; unpack8(*(const v4u*)(PLE + (size_t)t * D + lane2 * 32 + hh * 8), pl);
;             float z8[8]; unpack8(*(const v4u*)(ZB + (size_t)t * D + lane2 * 32 + hh * 8), z8);
;             f32x4 xa = (f32x4){z8[0], z8[1], z8[2], z8[3]}, xb = (f32x4){z8[4], z8[5], z8[6], z8[7]};
;             xa = (xa - mean1) * rstd1 * *(const f32x4*)(gain1 + lane2 * 32 + hh * 8) + *(const f32x4*)(bias1 + lane2 * 32 + hh * 8);
;             xb = (xb - mean1) * rstd1 * *(const f32x4*)(gain1 + lane2 * 32 + hh * 8 + 4) + *(const f32x4*)(bias1 + lane2 * 32 + hh * 8 + 4);
;             acc[hh * 4 + 0] += (f32x2){ALPHA * xa[0] + pl[0], ALPHA * xa[1] + pl[1]}; acc[hh * 4 + 1] += (f32x2){ALPHA * xa[2] + pl[2], ALPHA * xa[3] + pl[3]};
;             acc[hh * 4 + 2] += (f32x2){ALPHA * xb[0] + pl[4], ALPHA * xb[1] + pl[5]}; acc[hh * 4 + 3] += (f32x2){ALPHA * xb[2] + pl[6], ALPHA * xb[3] + pl[7]};
	s_waitcnt lgkmcnt(0)
	v_add_f32_e32 v78, v103, v104
	v_cvt_i32_f32_e32 v78, v78
	v_mov_b32_e32 v201, v130
	s_lshl_b64 s[56:57], s[86:87], 1
	v_lshlrev_b32_e32 v78, 3, v78
	v_sub_u32_e32 v78, 0, v78
	v_sub_u32_e32 v79, v78, v69
	v_add_u32_e32 v66, v79, v66
	v_sub_u32_e32 v79, v78, v70
	v_add_u32_e32 v74, v79, v74
	v_sub_u32_e32 v79, v78, v72
	v_add_u32_e32 v75, v79, v75
	v_sub_u32_e32 v79, v78, v73
	v_add_u32_e32 v76, v79, v76
	v_sub_u32_e32 v79, v78, v77
	v_add_u32_e32 v79, v79, v80
	v_sub_u32_e32 v80, v78, v81
	v_add_u32_e32 v80, v80, v85
	v_sub_u32_e32 v85, v78, v82
	v_add_u32_e32 v85, v85, v86
	v_sub_u32_e32 v86, v78, v84
	v_add_u32_e32 v86, v86, v94
	v_sub_u32_e32 v94, v78, v87
	v_add_u32_e32 v94, v94, v95
	v_sub_u32_e32 v95, v78, v88
	v_readlane_b32 s62, v255, 7
	v_lshlrev_b32_e32 v134, 5, v201
	v_add_u32_e32 v95, v95, v96
	v_sub_u32_e32 v96, v78, v89
	s_add_u32 s62, s62, s56
	v_readlane_b32 s63, v255, 9
	v_ashrrev_i32_e32 v135, 31, v134
	v_add_u32_e32 v96, v96, v97
	v_sub_u32_e32 v97, v78, v90
	v_cvt_f32_i32_e32 v181, v70
	v_mul_f32_e32 v142, 0x3c010204, v71
	s_addc_u32 s63, s63, s57
	v_lshlrev_b64 v[70:71], 1, v[134:135]
	v_add_u32_e32 v97, v97, v98
	v_sub_u32_e32 v98, v78, v91
	v_cvt_f32_i32_e32 v178, v75
	v_cvt_f32_i32_e32 v180, v74
	v_lshl_add_u64 v[74:75], s[62:63], 0, v[70:71]
	v_readlane_b32 s62, v254, 56
	v_add_u32_e32 v98, v98, v99
	v_sub_u32_e32 v99, v78, v92
	s_add_u32 s62, s62, s56
	v_readlane_b32 s63, v255, 5
	v_add_u32_e32 v99, v99, v100
	v_sub_u32_e32 v100, v78, v93
	v_sub_u32_e32 v78, v78, v83
	s_addc_u32 s63, s63, s57
	v_add_u32_e32 v100, v100, v101
	v_add_u32_e32 v78, v78, v102
	v_cvt_f32_i32_e32 v138, v99
	v_cvt_f32_i32_e32 v140, v98
	v_lshl_add_u64 v[98:99], s[62:63], 0, v[70:71]
	v_cvt_f32_i32_e32 v136, v100
	v_cvt_f32_i32_e32 v137, v93
	v_cvt_f32_i32_e32 v139, v92
	v_cvt_f32_i32_e32 v141, v91
	v_cvt_f32_i32_e32 v146, v97
	v_cvt_f32_i32_e32 v147, v90
	v_cvt_f32_i32_e32 v148, v96
	v_cvt_f32_i32_e32 v149, v89
	v_cvt_f32_i32_e32 v150, v95
	v_cvt_f32_i32_e32 v151, v88
	v_cvt_f32_i32_e32 v152, v94
	v_cvt_f32_i32_e32 v153, v87
	v_cvt_f32_i32_e32 v160, v86
	v_cvt_f32_i32_e32 v161, v84
	v_cvt_f32_i32_e32 v170, v85
	v_cvt_f32_i32_e32 v171, v82
	v_cvt_f32_i32_e32 v172, v80
	v_cvt_f32_i32_e32 v173, v81
	v_cvt_f32_i32_e32 v174, v79
	v_cvt_f32_i32_e32 v175, v77
	v_cvt_f32_i32_e32 v176, v76
	v_cvt_f32_i32_e32 v177, v73
	v_cvt_f32_i32_e32 v179, v72
	v_cvt_f32_i32_e32 v144, v78
	v_cvt_f32_i32_e32 v145, v83
	v_mov_b32_e32 v70, v212
	v_mov_b32_e32 v71, v213
	v_mov_b32_e32 v72, v214
	v_mov_b32_e32 v73, v215
	v_mov_b32_e32 v78, v216
	v_mov_b32_e32 v79, v217
	v_mov_b32_e32 v80, v218
	v_mov_b32_e32 v81, v219
	v_mov_b32_e32 v86, v220
	v_mov_b32_e32 v87, v221
	v_mov_b32_e32 v88, v222
	v_mov_b32_e32 v89, v223
	v_mov_b32_e32 v90, v224
	v_mov_b32_e32 v91, v225
	v_mov_b32_e32 v92, v226
	v_mov_b32_e32 v93, v227
	v_mov_b32_e32 v74, v228
	v_mov_b32_e32 v75, v229
	v_mov_b32_e32 v76, v230
	v_mov_b32_e32 v77, v231
	v_mov_b32_e32 v82, v232
	v_mov_b32_e32 v83, v233
	v_mov_b32_e32 v84, v234
	v_mov_b32_e32 v85, v235
	v_mov_b32_e32 v94, v236
	v_mov_b32_e32 v95, v237
	v_mov_b32_e32 v96, v238
	v_mov_b32_e32 v97, v239
	v_mov_b32_e32 v98, v240
	v_mov_b32_e32 v99, v241
	v_mov_b32_e32 v100, v242
	v_mov_b32_e32 v101, v243
	v_cvt_f32_i32_e32 v182, v66
	v_cvt_f32_i32_e32 v183, v69
	v_lshlrev_b64 v[154:155], 2, v[134:135]
	v_readlane_b32 s62, v255, 13
	v_lshl_add_u64 v[158:159], s[36:37], 0, v[154:155]
	v_readlane_b32 s63, v255, 14
	v_mul_f32_e32 v143, 0x3d800000, v142
	v_readlane_b32 s72, v254, 20
	v_lshl_add_u64 v[156:157], s[62:63], 0, v[154:155]
	v_readlane_b32 s73, v254, 21
	v_readlane_b32 s72, v255, 15
	v_readlane_b32 s73, v255, 16
	s_lshl_b64 s[62:63], s[86:87], 2
	v_readlane_b32 s74, v254, 22
	v_readlane_b32 s75, v254, 23
	s_add_u32 s62, s74, s62
	s_addc_u32 s63, s75, s63
	s_and_b64 vcc, exec, s[82:83]
	v_readlane_b32 s76, v254, 24
	v_readlane_b32 s77, v254, 25
	v_readlane_b32 s78, v254, 26
	v_readlane_b32 s79, v254, 27
	s_waitcnt vmcnt(0)
	v_readlane_b32 s98, v254, 58
	v_readlane_b32 s99, v255, 1
	s_cmp_lt_i32 s98, 0x4000
	s_cselect_b32 s100, s98, s88
	s_add_i32 s99, s98, s99
	s_cmp_lt_i32 s99, 0x4000
	s_cselect_b32 s99, s99, s100
	s_lshl_b32 s100, s100, 12
	s_lshl_b32 s99, s99, 9
	v_lshl_add_u32 v244, v130, 6, s100
	v_lshl_add_u32 v249, v130, 2, s99
	v_readlane_b32 s100, v255, 7
	v_readlane_b32 s101, v255, 9
	s_nop 4
	global_load_dwordx4 v[212:215], v244, s[100:101] offset:48
	global_load_dwordx4 v[216:219], v244, s[100:101] offset:32
	global_load_dwordx4 v[220:223], v244, s[100:101] offset:16
	global_load_dwordx4 v[224:227], v244, s[100:101]
	v_readlane_b32 s100, v254, 56
	v_readlane_b32 s101, v255, 5
	s_nop 4
	global_load_dwordx4 v[228:231], v244, s[100:101] offset:48
	global_load_dwordx4 v[232:235], v244, s[100:101] offset:32
	global_load_dwordx4 v[236:239], v244, s[100:101] offset:16
	global_load_dwordx4 v[240:243], v244, s[100:101]
	v_lshlrev_b32_e32 v66, 16, v98
	v_and_b32_e32 v69, 0xffff0000, v98
	v_lshlrev_b32_e32 v98, 16, v99
	v_and_b32_e32 v99, 0xffff0000, v99
	v_lshlrev_b32_e32 v164, 16, v100
	v_and_b32_e32 v165, 0xffff0000, v100
	v_lshlrev_b32_e32 v166, 16, v101
	v_and_b32_e32 v167, 0xffff0000, v101
	v_sub_f32_e32 v99, v99, v67
	v_sub_f32_e32 v98, v98, v67
	v_sub_f32_e32 v101, v69, v67
	v_sub_f32_e32 v100, v66, v67
	v_pk_mul_f32 v[184:185], v[68:69], v[100:101] op_sel_hi:[0,1]
	v_pk_mul_f32 v[186:187], v[68:69], v[98:99] op_sel_hi:[0,1]
	ds_read_b128 v[98:101], v154 offset:48
	ds_read_b128 v[102:105], v154 offset:32
	ds_read_b128 v[106:109], v154 offset:16
	ds_read_b128 v[122:125], v154 offset:0
	ds_read_b128 v[110:113], v154 offset:8240
	ds_read_b128 v[114:117], v154 offset:8224
	ds_read_b128 v[118:121], v154 offset:8208
	ds_read_b128 v[126:129], v154 offset:8192
	s_waitcnt lgkmcnt(0)
;     ...
;         for (int hh = 0; hh < 4; ++hh) { float pl[8]; unpack8(*(const v4u*)(PLE + (size_t)t * D + lane2 * 32 + hh * 8), pl);
;             float z8[8]; unpack8(*(const v4u*)(ZB + (size_t)t * D + lane2 * 32 + hh * 8), z8);
;             f32x4 xa = (f32x4){z8[0], z8[1], z8[2], z8[3]}, xb = (f32x4){z8[4], z8[5], z8[6], z8[7]};
;             xa = (xa - mean1) * rstd1 * *(const f32x4*)(gain1 + lane2 * 32 + hh * 8) + *(const f32x4*)(bias1 + lane2 * 32 + hh * 8);
;             xb = (xb - mean1) * rstd1 * *(const f32x4*)(gain1 + lane2 * 32 + hh * 8 + 4) + *(const f32x4*)(bias1 + lane2 * 32 + hh * 8 + 4);
;             acc[hh * 4 + 0] += (f32x2){ALPHA * xa[0] + pl[0], ALPHA * xa[1] + pl[1]}; acc[hh * 4 + 1] += (f32x2){ALPHA * xa[2] + pl[2], ALPHA * xa[3] + pl[3]};
;             acc[hh * 4 + 2] += (f32x2){ALPHA * xb[0] + pl[4], ALPHA * xb[1] + pl[5]}; acc[hh * 4 + 3] += (f32x2){ALPHA * xb[2] + pl[6], ALPHA * xb[3] + pl[7]};
; #pragma unroll
;             for (int i = 0; i < 4; ++i) s += acc[hh * 4 + i].x + acc[hh * 4 + i].y; }
	v_pk_fma_f32 v[124:125], v[124:125], v[186:187], v[128:129]
	v_sub_f32_e32 v129, v165, v67
	v_sub_f32_e32 v128, v164, v67
	v_pk_mul_f32 v[128:129], v[68:69], v[128:129] op_sel_hi:[0,1]
	v_pk_fma_f32 v[122:123], v[122:123], v[184:185], v[126:127]
	v_sub_f32_e32 v127, v167, v67
	v_sub_f32_e32 v126, v166, v67
	v_pk_fma_f32 v[106:107], v[106:107], v[128:129], v[118:119]
	v_lshlrev_b32_e32 v118, 16, v90
	v_and_b32_e32 v119, 0xffff0000, v90
	v_lshlrev_b32_e32 v90, 16, v91
	v_and_b32_e32 v91, 0xffff0000, v91
	v_pk_mul_f32 v[126:127], v[68:69], v[126:127] op_sel_hi:[0,1]
	v_pk_fma_f32 v[90:91], v[124:125], s[58:59], v[90:91] op_sel_hi:[1,0,1]
	v_pk_fma_f32 v[108:109], v[108:109], v[126:127], v[120:121]
	v_pk_fma_f32 v[118:119], v[122:123], s[58:59], v[118:119] op_sel_hi:[1,0,1]
	v_pk_fma_f32 v[120:121], v[142:143], v[180:181], v[90:91]
	v_lshlrev_b32_e32 v90, 16, v92
	v_and_b32_e32 v91, 0xffff0000, v92
	v_pk_fma_f32 v[118:119], v[142:143], v[182:183], v[118:119]
	v_pk_fma_f32 v[90:91], v[106:107], s[58:59], v[90:91] op_sel_hi:[1,0,1]
	v_add_f32_e32 v66, v118, v119
	v_pk_fma_f32 v[122:123], v[142:143], v[178:179], v[90:91]
	v_lshlrev_b32_e32 v90, 16, v93
	v_and_b32_e32 v91, 0xffff0000, v93
	v_pk_fma_f32 v[90:91], v[108:109], s[58:59], v[90:91] op_sel_hi:[1,0,1]
	v_add_f32_e32 v66, 0, v66
	v_add_f32_e32 v69, v120, v121
	v_pk_fma_f32 v[124:125], v[142:143], v[176:177], v[90:91]
	v_add_f32_e32 v66, v69, v66
	v_add_f32_e32 v69, v122, v123
	v_add_f32_e32 v66, v69, v66
	v_add_f32_e32 v69, v124, v125
	v_lshlrev_b32_e32 v90, 16, v95
	v_and_b32_e32 v91, 0xffff0000, v95
	v_lshlrev_b32_e32 v106, 16, v96
	v_and_b32_e32 v96, 0xffff0000, v96
	v_add_f32_e32 v66, v69, v66
	v_lshlrev_b32_e32 v69, 16, v94
	v_and_b32_e32 v92, 0xffff0000, v94
	v_lshlrev_b32_e32 v94, 16, v97
	v_and_b32_e32 v95, 0xffff0000, v97
	v_sub_f32_e32 v91, v91, v67
	v_sub_f32_e32 v90, v90, v67
	v_sub_f32_e32 v97, v96, v67
	v_sub_f32_e32 v96, v106, v67
	v_sub_f32_e32 v93, v92, v67
	v_sub_f32_e32 v92, v69, v67
	v_pk_mul_f32 v[90:91], v[68:69], v[90:91] op_sel_hi:[0,1]
	v_pk_mul_f32 v[96:97], v[68:69], v[96:97] op_sel_hi:[0,1]
	v_pk_mul_f32 v[92:93], v[68:69], v[92:93] op_sel_hi:[0,1]
	v_pk_fma_f32 v[90:91], v[104:105], v[90:91], v[116:117]
	v_pk_fma_f32 v[96:97], v[98:99], v[96:97], v[110:111]
	v_lshlrev_b32_e32 v98, 16, v86
	v_and_b32_e32 v99, 0xffff0000, v86
	v_lshlrev_b32_e32 v86, 16, v87
	v_and_b32_e32 v87, 0xffff0000, v87
	v_pk_fma_f32 v[92:93], v[102:103], v[92:93], v[114:115]
	v_pk_fma_f32 v[86:87], v[90:91], s[58:59], v[86:87] op_sel_hi:[1,0,1]
	v_sub_f32_e32 v95, v95, v67
	v_sub_f32_e32 v94, v94, v67
	v_pk_fma_f32 v[92:93], v[92:93], s[58:59], v[98:99] op_sel_hi:[1,0,1]
	v_pk_fma_f32 v[116:117], v[142:143], v[172:173], v[86:87]
	v_lshlrev_b32_e32 v86, 16, v88
	v_and_b32_e32 v87, 0xffff0000, v88
	v_pk_mul_f32 v[94:95], v[68:69], v[94:95] op_sel_hi:[0,1]
	v_pk_fma_f32 v[114:115], v[142:143], v[174:175], v[92:93]
	v_pk_fma_f32 v[86:87], v[96:97], s[58:59], v[86:87] op_sel_hi:[1,0,1]
	v_pk_fma_f32 v[94:95], v[100:101], v[94:95], v[112:113]
	v_pk_fma_f32 v[126:127], v[142:143], v[170:171], v[86:87]
	v_lshlrev_b32_e32 v86, 16, v89
	v_and_b32_e32 v87, 0xffff0000, v89
	v_add_f32_e32 v69, v114, v115
	v_pk_fma_f32 v[86:87], v[94:95], s[58:59], v[86:87] op_sel_hi:[1,0,1]
	v_add_f32_e32 v66, v66, v69
	v_add_f32_e32 v69, v116, v117
	v_pk_fma_f32 v[128:129], v[142:143], v[160:161], v[86:87]
	v_add_f32_e32 v66, v69, v66
	v_add_f32_e32 v69, v126, v127
	v_add_f32_e32 v66, v69, v66
	v_add_f32_e32 v69, v128, v129
	v_lshlrev_b32_e32 v86, 16, v82
	v_and_b32_e32 v87, 0xffff0000, v82
	v_lshlrev_b32_e32 v82, 16, v83
	v_and_b32_e32 v83, 0xffff0000, v83
	v_add_f32_e32 v66, v69, v66
	v_lshlrev_b32_e32 v69, 16, v84
	v_and_b32_e32 v172, 0xffff0000, v84
	v_lshlrev_b32_e32 v173, 16, v85
	v_and_b32_e32 v174, 0xffff0000, v85
	v_sub_f32_e32 v83, v83, v67
	v_sub_f32_e32 v82, v82, v67
	v_sub_f32_e32 v85, v87, v67
	v_sub_f32_e32 v84, v86, v67
	v_pk_mul_f32 v[160:161], v[68:69], v[84:85] op_sel_hi:[0,1]
	v_pk_mul_f32 v[170:171], v[68:69], v[82:83] op_sel_hi:[0,1]
	ds_read_b128 v[82:85], v154 offset:112
	ds_read_b128 v[86:89], v154 offset:96
	ds_read_b128 v[90:93], v154 offset:80
	ds_read_b128 v[106:109], v154 offset:64
	ds_read_b128 v[94:97], v154 offset:8304
	ds_read_b128 v[98:101], v154 offset:8288
	ds_read_b128 v[102:105], v154 offset:8272
	ds_read_b128 v[110:113], v154 offset:8256
	s_waitcnt lgkmcnt(0)
;     ...
;         for (int hh = 0; hh < 4; ++hh) { float pl[8]; unpack8(*(const v4u*)(PLE + (size_t)t * D + lane2 * 32 + hh * 8), pl);
;             float z8[8]; unpack8(*(const v4u*)(ZB + (size_t)t * D + lane2 * 32 + hh * 8), z8);
;             f32x4 xa = (f32x4){z8[0], z8[1], z8[2], z8[3]}, xb = (f32x4){z8[4], z8[5], z8[6], z8[7]};
;             xa = (xa - mean1) * rstd1 * *(const f32x4*)(gain1 + lane2 * 32 + hh * 8) + *(const f32x4*)(bias1 + lane2 * 32 + hh * 8);
;             xb = (xb - mean1) * rstd1 * *(const f32x4*)(gain1 + lane2 * 32 + hh * 8 + 4) + *(const f32x4*)(bias1 + lane2 * 32 + hh * 8 + 4);
;             acc[hh * 4 + 0] += (f32x2){ALPHA * xa[0] + pl[0], ALPHA * xa[1] + pl[1]}; acc[hh * 4 + 1] += (f32x2){ALPHA * xa[2] + pl[2], ALPHA * xa[3] + pl[3]};
;             acc[hh * 4 + 2] += (f32x2){ALPHA * xb[0] + pl[4], ALPHA * xb[1] + pl[5]}; acc[hh * 4 + 3] += (f32x2){ALPHA * xb[2] + pl[6], ALPHA * xb[3] + pl[7]};
; #pragma unroll
;             for (int i = 0; i < 4; ++i) s += acc[hh * 4 + i].x + acc[hh * 4 + i].y; }
;         const float mean = wave_sum(s) * (1.0f / D); float q = 0.f;
	v_pk_fma_f32 v[108:109], v[108:109], v[170:171], v[112:113]
	v_sub_f32_e32 v113, v172, v67
	v_sub_f32_e32 v112, v69, v67
	v_pk_mul_f32 v[112:113], v[68:69], v[112:113] op_sel_hi:[0,1]
	v_pk_fma_f32 v[106:107], v[106:107], v[160:161], v[110:111]
	v_sub_f32_e32 v111, v174, v67
	v_sub_f32_e32 v110, v173, v67
	v_pk_fma_f32 v[90:91], v[90:91], v[112:113], v[102:103]
	v_lshlrev_b32_e32 v102, 16, v78
	v_and_b32_e32 v103, 0xffff0000, v78
	v_lshlrev_b32_e32 v78, 16, v79
	v_and_b32_e32 v79, 0xffff0000, v79
	v_pk_mul_f32 v[110:111], v[68:69], v[110:111] op_sel_hi:[0,1]
	v_pk_fma_f32 v[78:79], v[108:109], s[58:59], v[78:79] op_sel_hi:[1,0,1]
	v_pk_fma_f32 v[92:93], v[92:93], v[110:111], v[104:105]
	v_pk_fma_f32 v[102:103], v[106:107], s[58:59], v[102:103] op_sel_hi:[1,0,1]
	v_pk_fma_f32 v[104:105], v[142:143], v[150:151], v[78:79]
	v_lshlrev_b32_e32 v78, 16, v80
	v_and_b32_e32 v79, 0xffff0000, v80
	v_pk_fma_f32 v[102:103], v[142:143], v[152:153], v[102:103]
	v_pk_fma_f32 v[78:79], v[90:91], s[58:59], v[78:79] op_sel_hi:[1,0,1]
	v_add_f32_e32 v69, v102, v103
	v_pk_fma_f32 v[90:91], v[142:143], v[148:149], v[78:79]
	v_lshlrev_b32_e32 v78, 16, v81
	v_and_b32_e32 v79, 0xffff0000, v81
	v_pk_fma_f32 v[78:79], v[92:93], s[58:59], v[78:79] op_sel_hi:[1,0,1]
	v_add_f32_e32 v66, v66, v69
	v_add_f32_e32 v69, v104, v105
	v_pk_fma_f32 v[92:93], v[142:143], v[146:147], v[78:79]
	v_add_f32_e32 v66, v69, v66
	v_add_f32_e32 v69, v90, v91
	v_add_f32_e32 v66, v69, v66
	v_add_f32_e32 v69, v92, v93
	v_add_f32_e32 v106, v69, v66
	v_lshlrev_b32_e32 v66, 16, v74
	v_and_b32_e32 v69, 0xffff0000, v74
	v_lshlrev_b32_e32 v74, 16, v75
	v_and_b32_e32 v75, 0xffff0000, v75
	v_lshlrev_b32_e32 v80, 16, v76
	v_and_b32_e32 v81, 0xffff0000, v76
	v_lshlrev_b32_e32 v78, 16, v77
	v_and_b32_e32 v79, 0xffff0000, v77
	v_sub_f32_e32 v75, v75, v67
	v_sub_f32_e32 v74, v74, v67
	v_sub_f32_e32 v77, v69, v67
	v_sub_f32_e32 v76, v66, v67
	v_pk_mul_f32 v[74:75], v[68:69], v[74:75] op_sel_hi:[0,1]
	v_sub_f32_e32 v79, v79, v67
	v_sub_f32_e32 v78, v78, v67
	v_sub_f32_e32 v81, v81, v67
	v_sub_f32_e32 v80, v80, v67
	v_pk_mul_f32 v[76:77], v[68:69], v[76:77] op_sel_hi:[0,1]
	v_pk_fma_f32 v[74:75], v[88:89], v[74:75], v[100:101]
	v_pk_mul_f32 v[66:67], v[68:69], v[80:81] op_sel_hi:[0,1]
	v_pk_mul_f32 v[68:69], v[68:69], v[78:79] op_sel_hi:[0,1]
	v_lshlrev_b32_e32 v78, 16, v70
	v_and_b32_e32 v79, 0xffff0000, v70
	v_lshlrev_b32_e32 v70, 16, v71
	v_and_b32_e32 v71, 0xffff0000, v71
	v_pk_fma_f32 v[76:77], v[86:87], v[76:77], v[98:99]
	v_pk_fma_f32 v[70:71], v[74:75], s[58:59], v[70:71] op_sel_hi:[1,0,1]
	v_pk_fma_f32 v[68:69], v[84:85], v[68:69], v[96:97]
	v_pk_fma_f32 v[66:67], v[82:83], v[66:67], v[94:95]
	v_pk_fma_f32 v[76:77], v[76:77], s[58:59], v[78:79] op_sel_hi:[1,0,1]
	v_pk_fma_f32 v[96:97], v[142:143], v[138:139], v[70:71]
	v_lshlrev_b32_e32 v70, 16, v72
	v_and_b32_e32 v71, 0xffff0000, v72
	v_pk_fma_f32 v[94:95], v[142:143], v[140:141], v[76:77]
	v_pk_fma_f32 v[66:67], v[66:67], s[58:59], v[70:71] op_sel_hi:[1,0,1]
	v_lshlrev_b32_e32 v70, 16, v73
	v_and_b32_e32 v71, 0xffff0000, v73
	v_pk_fma_f32 v[68:69], v[68:69], s[58:59], v[70:71] op_sel_hi:[1,0,1]
	v_mov_b32_e32 v70, v96
	v_mov_b32_e32 v71, v94
	v_mov_b32_e32 v72, v97
	v_mov_b32_e32 v73, v95
	v_pk_add_f32 v[70:71], v[70:71], v[72:73]
	v_pk_fma_f32 v[66:67], v[142:143], v[136:137], v[66:67]
	v_pk_fma_f32 v[68:69], v[142:143], v[144:145], v[68:69]
	v_add_f32_e32 v71, v106, v71
	v_add_f32_e32 v74, v70, v71
	v_mov_b32_e32 v70, v68
	v_mov_b32_e32 v71, v66
	v_mov_b32_e32 v72, v69
	v_mov_b32_e32 v73, v67
	v_pk_add_f32 v[70:71], v[70:71], v[72:73]
	v_lshl_add_u64 v[100:101], s[72:73], 0, v[154:155]
	v_add_f32_e32 v71, v71, v74
	v_add_f32_e32 v70, v70, v71
	v_mov_b32_e32 v71, v1
	v_lshl_add_u64 v[98:99], s[62:63], 0, v[154:155]
	v_mbcnt_lo_u32_b32 v71, -1, v71
	v_mbcnt_hi_u32_b32 v71, -1, v71
	v_lshlrev_b32_e32 v71, 2, v71
	v_xor_b32_e32 v72, 0x80, v71
	ds_bpermute_b32 v72, v72, v70
	s_waitcnt lgkmcnt(0)
	v_add_f32_e32 v70, v70, v72
	v_xor_b32_e32 v72, 64, v71
	ds_bpermute_b32 v72, v72, v70
	s_waitcnt lgkmcnt(0)
	v_add_f32_e32 v70, v70, v72
	v_xor_b32_e32 v72, 32, v71
	ds_bpermute_b32 v72, v72, v70
	s_waitcnt lgkmcnt(0)
	v_add_f32_e32 v70, v70, v72
	v_xor_b32_e32 v72, 16, v71
	ds_bpermute_b32 v72, v72, v70
	s_waitcnt lgkmcnt(0)
	v_add_f32_e32 v70, v70, v72
	v_xor_b32_e32 v72, 8, v71
	ds_bpermute_b32 v72, v72, v70
	v_xor_b32_e32 v71, 4, v71
	s_waitcnt lgkmcnt(0)
	v_add_f32_e32 v70, v70, v72
	ds_bpermute_b32 v71, v71, v70
	s_waitcnt lgkmcnt(0)
; __device__ __forceinline__ float ln_rstd(float q) { return __builtin_amdgcn_rsqf((q + LN_EPS * (float)D) * (1.0f / D)); }
;     ...
;         const float mean = wave_sum(s) * (1.0f / D); float q = 0.f;
; #pragma unroll
;         for (int i = 0; i < 16; ++i) { acc[i].x -= mean; acc[i].y -= mean; q += acc[i].x * acc[i].x + acc[i].y * acc[i].y; }
;         const float rstd = ln_rstd(wave_sum(q));
; #pragma unroll
;         for (int hh = 0; hh < 4; ++hh) {
;             const int c = lane2 * 32 + hh * 8;
;             float y[8];
; #pragma unroll
;             for (int q4 = 0; q4 < 2; ++q4) { const f32x4 ga = *(const f32x4*)(gain + c + q4 * 4), ba = *(const f32x4*)(bias + c + q4 * 4);
;                 const f32x2 z0 = acc[hh * 4 + q4 * 2], z1 = acc[hh * 4 + q4 * 2 + 1];
;                 f32x4 yo; yo[0] = z0.x * rstd * ga[0] + ba[0]; yo[1] = z0.y * rstd * ga[1] + ba[1]; yo[2] = z1.x * rstd * ga[2] + ba[2]; yo[3] = z1.y * rstd * ga[3] + ba[3];
;                 if (OF) *(f32x4*)(OF + (size_t)t * D + c + q4 * 4) = yo;
;                 y[q4 * 4] = yo[0]; y[q4 * 4 + 1] = yo[1]; y[q4 * 4 + 2] = yo[2]; y[q4 * 4 + 3] = yo[3]; }
	v_add_f32_e32 v70, v70, v71
	v_mul_f32_e32 v110, 0x3a000000, v70
	v_pk_add_f32 v[86:87], v[90:91], v[110:111] op_sel_hi:[1,0] neg_lo:[0,1] neg_hi:[0,1]
	v_pk_add_f32 v[88:89], v[92:93], v[110:111] op_sel_hi:[1,0] neg_lo:[0,1] neg_hi:[0,1]
	v_pk_add_f32 v[90:91], v[94:95], v[110:111] op_sel_hi:[1,0] neg_lo:[0,1] neg_hi:[0,1]
	v_pk_add_f32 v[92:93], v[96:97], v[110:111] op_sel_hi:[1,0] neg_lo:[0,1] neg_hi:[0,1]
	v_pk_add_f32 v[96:97], v[66:67], v[110:111] op_sel_hi:[1,0] neg_lo:[0,1] neg_hi:[0,1]
	v_pk_add_f32 v[94:95], v[68:69], v[110:111] op_sel_hi:[1,0] neg_lo:[0,1] neg_hi:[0,1]
	v_mov_b32_e32 v69, v97
	v_mov_b32_e32 v68, v95
	v_mov_b32_e32 v66, v94
	v_mov_b32_e32 v67, v96
	v_pk_mul_f32 v[68:69], v[68:69], v[68:69]
	v_pk_add_f32 v[82:83], v[102:103], v[110:111] op_sel_hi:[1,0] neg_lo:[0,1] neg_hi:[0,1]
	v_pk_fma_f32 v[144:145], v[66:67], v[66:67], v[68:69]
	v_mov_b32_e32 v66, v1
	v_lshl_add_u64 v[102:103], s[80:81], 0, v[154:155]
	v_mbcnt_lo_u32_b32 v66, -1, v66
	v_mbcnt_hi_u32_b32 v66, -1, v66
	v_lshlrev_b32_e32 v66, 2, v66
	v_xor_b32_e32 v148, 0x80, v66
	v_xor_b32_e32 v149, 64, v66
	v_xor_b32_e32 v150, 32, v66
	v_xor_b32_e32 v151, 16, v66
	v_xor_b32_e32 v152, 8, v66
	v_xor_b32_e32 v153, 4, v66
	ds_read_b128 v[66:69], v154 offset:16384
	ds_read_b128 v[106:109], v154 offset:24576
	v_pk_add_f32 v[70:71], v[122:123], v[110:111] op_sel_hi:[1,0] neg_lo:[0,1] neg_hi:[0,1]
	v_pk_add_f32 v[72:73], v[124:125], v[110:111] op_sel_hi:[1,0] neg_lo:[0,1] neg_hi:[0,1]
	v_pk_add_f32 v[74:75], v[114:115], v[110:111] op_sel_hi:[1,0] neg_lo:[0,1] neg_hi:[0,1]
	v_pk_add_f32 v[76:77], v[116:117], v[110:111] op_sel_hi:[1,0] neg_lo:[0,1] neg_hi:[0,1]
	v_pk_add_f32 v[78:79], v[126:127], v[110:111] op_sel_hi:[1,0] neg_lo:[0,1] neg_hi:[0,1]
	v_pk_add_f32 v[80:81], v[128:129], v[110:111] op_sel_hi:[1,0] neg_lo:[0,1] neg_hi:[0,1]
	v_pk_add_f32 v[84:85], v[104:105], v[110:111] op_sel_hi:[1,0] neg_lo:[0,1] neg_hi:[0,1]
	v_pk_add_f32 v[118:119], v[118:119], v[110:111] op_sel_hi:[1,0] neg_lo:[0,1] neg_hi:[0,1]
	v_pk_add_f32 v[110:111], v[120:121], v[110:111] op_sel_hi:[1,0] neg_lo:[0,1] neg_hi:[0,1]
	v_pk_mul_f32 v[146:147], v[118:119], v[118:119]
	v_pk_mul_f32 v[120:121], v[110:111], v[110:111]
	v_pk_mul_f32 v[112:113], v[70:71], v[70:71]
	v_add_f32_e32 v120, v120, v121
	v_add_f32_e32 v121, v146, v147
	v_pk_mul_f32 v[122:123], v[72:73], v[72:73]
	v_add_f32_e32 v120, v121, v120
	v_add_f32_e32 v112, v112, v113
	v_pk_mul_f32 v[114:115], v[74:75], v[74:75]
	v_add_f32_e32 v112, v112, v120
	v_add_f32_e32 v113, v122, v123
	v_pk_mul_f32 v[116:117], v[76:77], v[76:77]
	v_add_f32_e32 v112, v113, v112
	v_add_f32_e32 v113, v114, v115
	v_pk_mul_f32 v[124:125], v[78:79], v[78:79]
	v_add_f32_e32 v112, v113, v112
	v_add_f32_e32 v113, v116, v117
	v_pk_mul_f32 v[126:127], v[80:81], v[80:81]
	v_add_f32_e32 v112, v113, v112
	v_add_f32_e32 v113, v124, v125
	v_pk_mul_f32 v[128:129], v[82:83], v[82:83]
	v_add_f32_e32 v112, v113, v112
	v_add_f32_e32 v113, v126, v127
	v_pk_mul_f32 v[104:105], v[84:85], v[84:85]
	v_add_f32_e32 v112, v113, v112
	v_add_f32_e32 v113, v128, v129
	v_pk_mul_f32 v[136:137], v[86:87], v[86:87]
	v_add_f32_e32 v112, v113, v112
	v_add_f32_e32 v104, v104, v105
	v_pk_mul_f32 v[138:139], v[88:89], v[88:89]
	v_add_f32_e32 v104, v104, v112
	v_add_f32_e32 v105, v136, v137
	v_pk_mul_f32 v[140:141], v[90:91], v[90:91]
	v_add_f32_e32 v104, v105, v104
	v_add_f32_e32 v105, v138, v139
	v_pk_mul_f32 v[142:143], v[92:93], v[92:93]
	v_add_f32_e32 v104, v105, v104
	v_add_f32_e32 v105, v140, v141
	v_add_f32_e32 v104, v105, v104
	v_add_f32_e32 v105, v142, v143
	v_add_f32_e32 v104, v105, v104
	v_add_f32_e32 v104, v145, v104
	v_add_f32_e32 v104, v144, v104
	ds_bpermute_b32 v105, v148, v104
	s_waitcnt lgkmcnt(0)
	v_add_f32_e32 v104, v104, v105
	ds_bpermute_b32 v105, v149, v104
	s_waitcnt lgkmcnt(0)
	v_add_f32_e32 v104, v104, v105
	ds_bpermute_b32 v105, v150, v104
	s_waitcnt lgkmcnt(0)
	v_add_f32_e32 v104, v104, v105
	ds_bpermute_b32 v105, v151, v104
	s_waitcnt lgkmcnt(0)
	v_add_f32_e32 v104, v104, v105
	ds_bpermute_b32 v105, v152, v104
	s_waitcnt lgkmcnt(0)
	v_add_f32_e32 v104, v104, v105
	ds_bpermute_b32 v105, v153, v104
	s_waitcnt lgkmcnt(0)
	v_add_f32_e32 v104, v104, v105
	v_add_f32_e32 v104, 0x3ca7c5ac, v104
	v_mul_f32_e32 v104, 0x3a000000, v104
	v_rsq_f32_e32 v104, v104
	s_nop 0
	v_pk_mul_f32 v[112:113], v[118:119], v[104:105] op_sel_hi:[1,0]
	s_nop 0
	v_pk_fma_f32 v[66:67], v[66:67], v[112:113], v[106:107]
	v_pk_mul_f32 v[106:107], v[110:111], v[104:105] op_sel_hi:[1,0]
	s_nop 0
	v_pk_fma_f32 v[68:69], v[68:69], v[106:107], v[108:109]
	s_cbranch_vccz .LBB0_1428
	global_store_dwordx4 v[98:99], v[66:69], off
